# static priority raise for waves 4-7 in the two router phases (on top of the RG-LRU raise)
# speedup vs baseline: 1.0039x; 1.0039x over previous
.LBB0_559:
	s_load_dwordx4 s[0:3], s[8:9], 0x138
	s_waitcnt lgkmcnt(0)
	s_mov_b64 s[4:5], s[0:1]
	s_cmp_lt_i32 s4, 6
	s_cselect_b64 s[0:1], -1, 0
	s_cmp_gt_i32 s5, 5
	s_cselect_b64 s[2:3], -1, 0
	s_and_b64 s[0:1], s[0:1], s[2:3]
	s_andn2_b64 vcc, exec, s[0:1]
	s_cbranch_vccnz .LBB0_740
	s_cmp_ge_u32 s33, 0x100
	s_cbranch_scc0 .Lrt_prio_a
	s_setprio 1
.Lrt_prio_a:
	s_mov_b64 s[4:5], s[8:9]
	v_mbcnt_lo_u32_b32 v92, -1, 0
	v_mbcnt_hi_u32_b32 v92, -1, v92
	s_load_dword s7, s[8:9], 0x148
	s_add_u32 s0, s8, 0x148
	s_addc_u32 s1, s9, 0
	v_writelane_b32 v242, s0, 41
	s_waitcnt vmcnt(0)
	v_add_u32_e32 v56, s33, v92
	s_waitcnt lgkmcnt(0)
	s_abs_i32 s6, s7
	v_cvt_f32_u32_e32 v0, s6
	v_writelane_b32 v242, s1, 42
	s_load_dwordx2 s[52:53], s[4:5], 0x130
	s_load_dwordx4 s[0:3], s[4:5], 0xe8
	v_lshlrev_b32_e32 v58, 2, v56
	v_rcp_iflag_f32_e32 v0, v0
	v_ashrrev_i32_e32 v59, 31, v58
	v_writelane_b32 v242, s7, 43
	s_ashr_i32 s4, s7, 31
	v_mul_f32_e32 v0, 0x4f7ffffe, v0
	v_cvt_u32_f32_e32 v0, v0
	s_waitcnt lgkmcnt(0)
	s_barrier
	v_readfirstlane_b32 s7, v0
	v_lshl_add_u64 v[0:1], v[58:59], 2, s[0:1]
	global_load_dwordx4 v[86:89], v[0:1], off
	v_add_u32_e32 v90, 0x800, v58
	v_ashrrev_i32_e32 v91, 31, v90
	v_lshl_add_u64 v[0:1], v[90:91], 2, s[0:1]
	global_load_dwordx4 v[94:97], v[0:1], off
	v_add_u32_e32 v98, 0x1000, v58
	v_add_u32_e32 v84, 0x1800, v58
	v_ashrrev_i32_e32 v99, 31, v98
	v_ashrrev_i32_e32 v85, 31, v84
	v_add_u32_e32 v82, 0x2000, v58
	v_add_u32_e32 v80, 0x2800, v58
	v_lshl_add_u64 v[0:1], v[98:99], 2, s[0:1]
	v_lshl_add_u64 v[2:3], v[84:85], 2, s[0:1]
	v_ashrrev_i32_e32 v83, 31, v82
	v_ashrrev_i32_e32 v81, 31, v80
	v_add_u32_e32 v78, 0x3000, v58
	v_add_u32_e32 v76, 0x3800, v58
	s_sub_i32 s5, 0, s6
	global_load_dwordx4 v[52:55], v[0:1], off
	global_load_dwordx4 v[48:51], v[2:3], off
	v_lshl_add_u64 v[0:1], v[82:83], 2, s[0:1]
	v_lshl_add_u64 v[2:3], v[80:81], 2, s[0:1]
	v_ashrrev_i32_e32 v79, 31, v78
	v_ashrrev_i32_e32 v77, 31, v76
	v_add_u32_e32 v74, 0x4000, v58
	v_add_u32_e32 v72, 0x4800, v58
	s_mul_i32 s5, s5, s7
	global_load_dwordx4 v[44:47], v[0:1], off
	global_load_dwordx4 v[40:43], v[2:3], off
	v_lshl_add_u64 v[0:1], v[78:79], 2, s[0:1]
	v_lshl_add_u64 v[2:3], v[76:77], 2, s[0:1]
	v_ashrrev_i32_e32 v75, 31, v74
	v_ashrrev_i32_e32 v73, 31, v72
	v_add_u32_e32 v70, 0x5000, v58
	v_add_u32_e32 v68, 0x5800, v58
	s_mul_hi_u32 s5, s7, s5
	global_load_dwordx4 v[36:39], v[0:1], off
	global_load_dwordx4 v[32:35], v[2:3], off
	v_lshl_add_u64 v[0:1], v[74:75], 2, s[0:1]
	v_lshl_add_u64 v[2:3], v[72:73], 2, s[0:1]
	v_ashrrev_i32_e32 v71, 31, v70
	v_ashrrev_i32_e32 v69, 31, v68
	v_add_u32_e32 v66, 0x6000, v58
	v_add_u32_e32 v64, 0x6800, v58
	v_add_u32_e32 v62, 0x7000, v58
	v_add_u32_e32 v60, 0x7800, v58
	s_add_i32 s7, s7, s5
	global_load_dwordx4 v[28:31], v[0:1], off
	global_load_dwordx4 v[24:27], v[2:3], off
	v_lshl_add_u64 v[0:1], v[70:71], 2, s[0:1]
	v_lshl_add_u64 v[2:3], v[68:69], 2, s[0:1]
	v_ashrrev_i32_e32 v67, 31, v66
	v_ashrrev_i32_e32 v65, 31, v64
	v_ashrrev_i32_e32 v63, 31, v62
	v_ashrrev_i32_e32 v61, 31, v60
	s_mul_hi_u32 s5, s7, 0x9000
	global_load_dwordx4 v[20:23], v[0:1], off
	global_load_dwordx4 v[16:19], v[2:3], off
	v_lshl_add_u64 v[0:1], v[66:67], 2, s[0:1]
	v_lshl_add_u64 v[2:3], v[64:65], 2, s[0:1]
	v_lshl_add_u64 v[100:101], v[62:63], 2, s[0:1]
	v_lshl_add_u64 v[102:103], v[60:61], 2, s[0:1]
	s_movk_i32 s0, 0x7fff
	s_mul_i32 s7, s5, s6
	s_sub_i32 s7, 0x9000, s7
	s_add_i32 s8, s5, 1
	s_sub_i32 s9, s7, s6
	s_cmp_ge_u32 s7, s6
	v_and_b32_e32 v65, 28, v58
	v_bfe_i32 v73, v56, 6, 24
	s_cselect_b32 s5, s8, s5
	v_lshrrev_b32_e32 v57, 2, v56
	v_bitop3_b32 v67, v58, v73, 12 bitop3:0x6c
	s_cselect_b32 s7, s9, s7
	s_add_i32 s8, s5, 1
	v_and_b32_e32 v57, 14, v57
	s_cmp_ge_u32 s7, s6
	s_cselect_b32 s5, s8, s5
	s_add_i32 s1, 0, 0x10000
	global_load_dwordx4 v[12:15], v[0:1], off
	global_load_dwordx4 v[8:11], v[2:3], off
	global_load_dwordx4 v[4:7], v[100:101], off
	s_nop 0
	global_load_dwordx4 v[0:3], v[102:103], off
	s_xor_b32 s5, s5, s4
	s_sub_i32 s18, s5, s4
	v_readlane_b32 s4, v243, 0
	v_readlane_b32 s5, v243, 1
	s_waitcnt vmcnt(15)
	v_bfe_u32 v59, v86, 16, 1
	v_add3_u32 v59, v86, v59, s0
	v_and_b32_e32 v61, 0xffff0000, v59
	v_sub_f32_e32 v61, v86, v61
	v_bfe_u32 v63, v61, 16, 1
	v_add3_u32 v61, v61, v63, s0
	v_lshlrev_b32_e32 v63, 11, v65
	v_lshl_add_u32 v67, v67, 4, v63
	v_or_b32_e32 v67, v67, v57
	v_add_u32_e32 v69, 0, v67
	ds_write_b16_d16_hi v69, v59
	v_add_u32_e32 v59, s1, v67
	ds_write_b16_d16_hi v59, v61
	v_bfe_u32 v61, v87, 16, 1
	v_add3_u32 v61, v87, v61, s0
	v_and_b32_e32 v67, 0xffff0000, v61
	v_sub_f32_e32 v67, v87, v67
	v_or_b32_e32 v59, 1, v65
	v_bfe_u32 v69, v67, 16, 1
	v_add3_u32 v69, v67, v69, s0
	v_lshlrev_b32_e32 v67, 11, v59
	v_bitop3_b32 v71, v59, v73, 13 bitop3:0x6c
	v_lshl_add_u32 v71, v71, 4, v67
	v_or_b32_e32 v71, v71, v57
	v_add_u32_e32 v75, 0, v71
	ds_write_b16_d16_hi v75, v61
	v_add_u32_e32 v61, s1, v71
	ds_write_b16_d16_hi v61, v69
	v_bfe_u32 v69, v88, 16, 1
	v_add3_u32 v71, v88, v69, s0
	v_and_b32_e32 v69, 0xffff0000, v71
	v_sub_f32_e32 v69, v88, v69
	v_or_b32_e32 v61, 2, v65
	v_bfe_u32 v75, v69, 16, 1
	v_add3_u32 v75, v69, v75, s0
	v_lshlrev_b32_e32 v69, 11, v61
	v_bitop3_b32 v77, v61, v73, 14 bitop3:0x6c
	v_lshl_add_u32 v77, v77, 4, v69
	v_or_b32_e32 v77, v77, v57
	v_add_u32_e32 v79, 0, v77
	ds_write_b16_d16_hi v79, v71
	v_add_u32_e32 v71, s1, v77
	ds_write_b16_d16_hi v71, v75
	v_bfe_u32 v71, v89, 16, 1
	v_add3_u32 v75, v89, v71, s0
	v_and_b32_e32 v71, 0xffff0000, v75
	v_sub_f32_e32 v71, v89, v71
	v_or_b32_e32 v65, 3, v65
	v_bfe_u32 v77, v71, 16, 1
	v_add3_u32 v77, v71, v77, s0
	v_lshlrev_b32_e32 v71, 11, v65
	v_bitop3_b32 v73, v65, v73, 15 bitop3:0x6c
	v_lshl_add_u32 v73, v73, 4, v71
	v_or_b32_e32 v73, v73, v57
	v_add_u32_e32 v79, 0, v73
	ds_write_b16_d16_hi v79, v75
	s_waitcnt vmcnt(14)
	v_bfe_u32 v75, v94, 16, 1
	v_add_u32_e32 v73, s1, v73
	v_add3_u32 v75, v94, v75, s0
	ds_write_b16_d16_hi v73, v77
	v_and_b32_e32 v77, 0xffff0000, v75
	v_sub_f32_e32 v77, v94, v77
	v_ashrrev_i32_e32 v73, 8, v90
	v_bfe_u32 v79, v77, 16, 1
	v_add3_u32 v77, v77, v79, s0
	v_bitop3_b32 v79, v73, v58, 12 bitop3:0x78
	v_lshl_add_u32 v79, v79, 4, v63
	v_or_b32_e32 v79, v79, v57
	v_add_u32_e32 v81, 0, v79
	ds_write_b16_d16_hi v81, v75
	v_add_u32_e32 v75, s1, v79
	ds_write_b16_d16_hi v75, v77
	v_bfe_u32 v75, v95, 16, 1
	v_add3_u32 v75, v95, v75, s0
	v_and_b32_e32 v77, 0xffff0000, v75
	v_sub_f32_e32 v77, v95, v77
	v_bfe_u32 v79, v77, 16, 1
	v_add3_u32 v77, v77, v79, s0
	v_bitop3_b32 v79, v59, v73, 13 bitop3:0x6c
	v_lshl_add_u32 v79, v79, 4, v67
	v_or_b32_e32 v79, v79, v57
	v_add_u32_e32 v81, 0, v79
	ds_write_b16_d16_hi v81, v75
	v_add_u32_e32 v75, s1, v79
	ds_write_b16_d16_hi v75, v77
	v_bfe_u32 v75, v96, 16, 1
	v_add3_u32 v75, v96, v75, s0
	v_and_b32_e32 v77, 0xffff0000, v75
	v_sub_f32_e32 v77, v96, v77
	v_bfe_u32 v79, v77, 16, 1
	v_add3_u32 v77, v77, v79, s0
	v_bitop3_b32 v79, v61, v73, 14 bitop3:0x6c
	v_lshl_add_u32 v79, v79, 4, v69
	v_or_b32_e32 v79, v79, v57
	v_add_u32_e32 v81, 0, v79
	ds_write_b16_d16_hi v81, v75
	v_add_u32_e32 v75, s1, v79
	ds_write_b16_d16_hi v75, v77
	v_bfe_u32 v75, v97, 16, 1
	v_add3_u32 v75, v97, v75, s0
	v_and_b32_e32 v77, 0xffff0000, v75
	v_bitop3_b32 v73, v65, v73, 15 bitop3:0x6c
	v_sub_f32_e32 v77, v97, v77
	v_lshl_add_u32 v73, v73, 4, v71
	v_bfe_u32 v79, v77, 16, 1
	v_or_b32_e32 v73, v73, v57
	v_add3_u32 v77, v77, v79, s0
	v_add_u32_e32 v79, 0, v73
	ds_write_b16_d16_hi v79, v75
	s_waitcnt vmcnt(13)
	v_bfe_u32 v75, v52, 16, 1
	v_add_u32_e32 v73, s1, v73
	v_add3_u32 v75, v52, v75, s0
	ds_write_b16_d16_hi v73, v77
	v_and_b32_e32 v77, 0xffff0000, v75
	v_sub_f32_e32 v52, v52, v77
	v_ashrrev_i32_e32 v73, 8, v98
	v_bfe_u32 v77, v52, 16, 1
	v_add3_u32 v52, v52, v77, s0
	v_bitop3_b32 v77, v73, v58, 12 bitop3:0x78
	v_lshl_add_u32 v77, v77, 4, v63
	v_or_b32_e32 v77, v77, v57
	v_add_u32_e32 v79, 0, v77
	ds_write_b16_d16_hi v79, v75
	v_add_u32_e32 v75, s1, v77
	ds_write_b16_d16_hi v75, v52
	v_bfe_u32 v52, v53, 16, 1
	v_add3_u32 v52, v53, v52, s0
	v_and_b32_e32 v75, 0xffff0000, v52
	v_sub_f32_e32 v53, v53, v75
	v_bfe_u32 v75, v53, 16, 1
	v_add3_u32 v53, v53, v75, s0
	v_bitop3_b32 v75, v59, v73, 13 bitop3:0x6c
	v_lshl_add_u32 v75, v75, 4, v67
	v_or_b32_e32 v75, v75, v57
	v_add_u32_e32 v77, 0, v75
	ds_write_b16_d16_hi v77, v52
	v_add_u32_e32 v52, s1, v75
	ds_write_b16_d16_hi v52, v53
	v_bfe_u32 v52, v54, 16, 1
	v_add3_u32 v52, v54, v52, s0
	v_and_b32_e32 v53, 0xffff0000, v52
	v_sub_f32_e32 v53, v54, v53
	v_bfe_u32 v54, v53, 16, 1
	v_add3_u32 v53, v53, v54, s0
	v_bitop3_b32 v54, v61, v73, 14 bitop3:0x6c
	v_lshl_add_u32 v54, v54, 4, v69
	v_or_b32_e32 v54, v54, v57
	v_add_u32_e32 v75, 0, v54
	ds_write_b16_d16_hi v75, v52
	v_add_u32_e32 v52, s1, v54
	ds_write_b16_d16_hi v52, v53
	v_bfe_u32 v52, v55, 16, 1
	v_add3_u32 v52, v55, v52, s0
	v_and_b32_e32 v53, 0xffff0000, v52
	v_sub_f32_e32 v53, v55, v53
	v_bfe_u32 v54, v53, 16, 1
	v_add3_u32 v53, v53, v54, s0
	v_bitop3_b32 v54, v65, v73, 15 bitop3:0x6c
	v_lshl_add_u32 v54, v54, 4, v71
	v_or_b32_e32 v54, v54, v57
	v_add_u32_e32 v55, 0, v54
	ds_write_b16_d16_hi v55, v52
	v_add_u32_e32 v52, s1, v54
	ds_write_b16_d16_hi v52, v53
	s_waitcnt vmcnt(12)
	v_bfe_u32 v53, v48, 16, 1
	v_add3_u32 v53, v48, v53, s0
	v_and_b32_e32 v54, 0xffff0000, v53
	v_sub_f32_e32 v48, v48, v54
	v_ashrrev_i32_e32 v52, 8, v84
	v_bfe_u32 v54, v48, 16, 1
	v_add3_u32 v48, v48, v54, s0
	v_bitop3_b32 v54, v52, v58, 12 bitop3:0x78
	v_lshl_add_u32 v54, v54, 4, v63
	v_or_b32_e32 v54, v54, v57
	v_add_u32_e32 v55, 0, v54
	ds_write_b16_d16_hi v55, v53
	v_add_u32_e32 v53, s1, v54
	ds_write_b16_d16_hi v53, v48
	v_bfe_u32 v48, v49, 16, 1
	v_add3_u32 v48, v49, v48, s0
	v_and_b32_e32 v53, 0xffff0000, v48
	v_sub_f32_e32 v49, v49, v53
	v_bfe_u32 v53, v49, 16, 1
	v_add3_u32 v49, v49, v53, s0
	v_bitop3_b32 v53, v59, v52, 13 bitop3:0x6c
	v_lshl_add_u32 v53, v53, 4, v67
	v_or_b32_e32 v53, v53, v57
	v_add_u32_e32 v54, 0, v53
	ds_write_b16_d16_hi v54, v48
	v_add_u32_e32 v48, s1, v53
	ds_write_b16_d16_hi v48, v49
	v_bfe_u32 v48, v50, 16, 1
	v_add3_u32 v48, v50, v48, s0
	v_and_b32_e32 v49, 0xffff0000, v48
	v_sub_f32_e32 v49, v50, v49
	v_bfe_u32 v50, v49, 16, 1
	v_add3_u32 v49, v49, v50, s0
	v_bitop3_b32 v50, v61, v52, 14 bitop3:0x6c
	v_lshl_add_u32 v50, v50, 4, v69
	v_or_b32_e32 v50, v50, v57
	v_add_u32_e32 v53, 0, v50
	ds_write_b16_d16_hi v53, v48
	v_add_u32_e32 v48, s1, v50
	ds_write_b16_d16_hi v48, v49
	v_bfe_u32 v48, v51, 16, 1
	v_add3_u32 v48, v51, v48, s0
	v_and_b32_e32 v49, 0xffff0000, v48
	v_sub_f32_e32 v49, v51, v49
	v_bfe_u32 v50, v49, 16, 1
	v_add3_u32 v49, v49, v50, s0
	v_bitop3_b32 v50, v65, v52, 15 bitop3:0x6c
	v_lshl_add_u32 v50, v50, 4, v71
	v_or_b32_e32 v50, v50, v57
	v_add_u32_e32 v51, 0, v50
	ds_write_b16_d16_hi v51, v48
	v_add_u32_e32 v48, s1, v50
	ds_write_b16_d16_hi v48, v49
	s_waitcnt vmcnt(11)
	v_bfe_u32 v49, v44, 16, 1
	v_add3_u32 v49, v44, v49, s0
	v_and_b32_e32 v50, 0xffff0000, v49
	v_sub_f32_e32 v44, v44, v50
	v_ashrrev_i32_e32 v48, 8, v82
	v_bfe_u32 v50, v44, 16, 1
	v_add3_u32 v44, v44, v50, s0
	v_bitop3_b32 v50, v48, v58, 12 bitop3:0x78
	v_lshl_add_u32 v50, v50, 4, v63
	v_or_b32_e32 v50, v50, v57
	v_add_u32_e32 v51, 0, v50
	ds_write_b16_d16_hi v51, v49
	v_add_u32_e32 v49, s1, v50
	ds_write_b16_d16_hi v49, v44
	v_bfe_u32 v44, v45, 16, 1
	v_add3_u32 v44, v45, v44, s0
	v_and_b32_e32 v49, 0xffff0000, v44
	v_sub_f32_e32 v45, v45, v49
	v_bfe_u32 v49, v45, 16, 1
	v_add3_u32 v45, v45, v49, s0
	v_bitop3_b32 v49, v59, v48, 13 bitop3:0x6c
	v_lshl_add_u32 v49, v49, 4, v67
	v_or_b32_e32 v49, v49, v57
	v_add_u32_e32 v50, 0, v49
	ds_write_b16_d16_hi v50, v44
	v_add_u32_e32 v44, s1, v49
	ds_write_b16_d16_hi v44, v45
	v_bfe_u32 v44, v46, 16, 1
	v_add3_u32 v44, v46, v44, s0
	v_and_b32_e32 v45, 0xffff0000, v44
	v_sub_f32_e32 v45, v46, v45
	v_bfe_u32 v46, v45, 16, 1
	v_add3_u32 v45, v45, v46, s0
	v_bitop3_b32 v46, v61, v48, 14 bitop3:0x6c
	v_lshl_add_u32 v46, v46, 4, v69
	v_or_b32_e32 v46, v46, v57
	v_add_u32_e32 v49, 0, v46
	ds_write_b16_d16_hi v49, v44
	v_add_u32_e32 v44, s1, v46
	ds_write_b16_d16_hi v44, v45
	v_bfe_u32 v44, v47, 16, 1
	v_add3_u32 v44, v47, v44, s0
	v_and_b32_e32 v45, 0xffff0000, v44
	v_sub_f32_e32 v45, v47, v45
	v_bfe_u32 v46, v45, 16, 1
	v_add3_u32 v45, v45, v46, s0
	v_bitop3_b32 v46, v65, v48, 15 bitop3:0x6c
	v_lshl_add_u32 v46, v46, 4, v71
	v_or_b32_e32 v46, v46, v57
	v_add_u32_e32 v47, 0, v46
	ds_write_b16_d16_hi v47, v44
	v_add_u32_e32 v44, s1, v46
	ds_write_b16_d16_hi v44, v45
	s_waitcnt vmcnt(10)
	v_bfe_u32 v45, v40, 16, 1
	v_add3_u32 v45, v40, v45, s0
	v_and_b32_e32 v46, 0xffff0000, v45
	v_sub_f32_e32 v40, v40, v46
	v_ashrrev_i32_e32 v44, 8, v80
	v_bfe_u32 v46, v40, 16, 1
	v_add3_u32 v40, v40, v46, s0
	v_bitop3_b32 v46, v44, v58, 12 bitop3:0x78
	v_lshl_add_u32 v46, v46, 4, v63
	v_or_b32_e32 v46, v46, v57
	v_add_u32_e32 v47, 0, v46
	ds_write_b16_d16_hi v47, v45
	v_add_u32_e32 v45, s1, v46
	ds_write_b16_d16_hi v45, v40
	v_bfe_u32 v40, v41, 16, 1
	v_add3_u32 v40, v41, v40, s0
	v_and_b32_e32 v45, 0xffff0000, v40
	v_sub_f32_e32 v41, v41, v45
	v_bfe_u32 v45, v41, 16, 1
	v_add3_u32 v41, v41, v45, s0
	v_bitop3_b32 v45, v59, v44, 13 bitop3:0x6c
	v_lshl_add_u32 v45, v45, 4, v67
	v_or_b32_e32 v45, v45, v57
	v_add_u32_e32 v46, 0, v45
	ds_write_b16_d16_hi v46, v40
	v_add_u32_e32 v40, s1, v45
	ds_write_b16_d16_hi v40, v41
	v_bfe_u32 v40, v42, 16, 1
	v_add3_u32 v40, v42, v40, s0
	v_and_b32_e32 v41, 0xffff0000, v40
	v_sub_f32_e32 v41, v42, v41
	v_bfe_u32 v42, v41, 16, 1
	v_add3_u32 v41, v41, v42, s0
	v_bitop3_b32 v42, v61, v44, 14 bitop3:0x6c
	v_lshl_add_u32 v42, v42, 4, v69
	v_or_b32_e32 v42, v42, v57
	v_add_u32_e32 v45, 0, v42
	ds_write_b16_d16_hi v45, v40
	v_add_u32_e32 v40, s1, v42
	ds_write_b16_d16_hi v40, v41
	v_bfe_u32 v40, v43, 16, 1
	v_add3_u32 v40, v43, v40, s0
	v_and_b32_e32 v41, 0xffff0000, v40
	v_sub_f32_e32 v41, v43, v41
	v_bfe_u32 v42, v41, 16, 1
	v_add3_u32 v41, v41, v42, s0
	v_bitop3_b32 v42, v65, v44, 15 bitop3:0x6c
	v_lshl_add_u32 v42, v42, 4, v71
	v_or_b32_e32 v42, v42, v57
	v_add_u32_e32 v43, 0, v42
	ds_write_b16_d16_hi v43, v40
	v_add_u32_e32 v40, s1, v42
	ds_write_b16_d16_hi v40, v41
	s_waitcnt vmcnt(9)
	v_bfe_u32 v41, v36, 16, 1
	v_add3_u32 v41, v36, v41, s0
	v_and_b32_e32 v42, 0xffff0000, v41
	v_sub_f32_e32 v36, v36, v42
	v_ashrrev_i32_e32 v40, 8, v78
	v_bfe_u32 v42, v36, 16, 1
	v_add3_u32 v36, v36, v42, s0
	v_bitop3_b32 v42, v40, v58, 12 bitop3:0x78
	v_lshl_add_u32 v42, v42, 4, v63
	v_or_b32_e32 v42, v42, v57
	v_add_u32_e32 v43, 0, v42
	ds_write_b16_d16_hi v43, v41
	v_add_u32_e32 v41, s1, v42
	ds_write_b16_d16_hi v41, v36
	v_bfe_u32 v36, v37, 16, 1
	v_add3_u32 v36, v37, v36, s0
	v_and_b32_e32 v41, 0xffff0000, v36
	v_sub_f32_e32 v37, v37, v41
	v_bfe_u32 v41, v37, 16, 1
	v_add3_u32 v37, v37, v41, s0
	v_bitop3_b32 v41, v59, v40, 13 bitop3:0x6c
	v_lshl_add_u32 v41, v41, 4, v67
	v_or_b32_e32 v41, v41, v57
	v_add_u32_e32 v42, 0, v41
	ds_write_b16_d16_hi v42, v36
	v_add_u32_e32 v36, s1, v41
	ds_write_b16_d16_hi v36, v37
	v_bfe_u32 v36, v38, 16, 1
	v_add3_u32 v36, v38, v36, s0
	v_and_b32_e32 v37, 0xffff0000, v36
	v_sub_f32_e32 v37, v38, v37
	v_bfe_u32 v38, v37, 16, 1
	v_add3_u32 v37, v37, v38, s0
	v_bitop3_b32 v38, v61, v40, 14 bitop3:0x6c
	v_lshl_add_u32 v38, v38, 4, v69
	v_or_b32_e32 v38, v38, v57
	v_add_u32_e32 v41, 0, v38
	ds_write_b16_d16_hi v41, v36
	v_add_u32_e32 v36, s1, v38
	ds_write_b16_d16_hi v36, v37
	v_bfe_u32 v36, v39, 16, 1
	v_add3_u32 v36, v39, v36, s0
	v_and_b32_e32 v37, 0xffff0000, v36
	v_sub_f32_e32 v37, v39, v37
	v_bfe_u32 v38, v37, 16, 1
	v_add3_u32 v37, v37, v38, s0
	v_bitop3_b32 v38, v65, v40, 15 bitop3:0x6c
	v_lshl_add_u32 v38, v38, 4, v71
	v_or_b32_e32 v38, v38, v57
	v_add_u32_e32 v39, 0, v38
	ds_write_b16_d16_hi v39, v36
	v_add_u32_e32 v36, s1, v38
	ds_write_b16_d16_hi v36, v37
	s_waitcnt vmcnt(8)
	v_bfe_u32 v37, v32, 16, 1
	v_add3_u32 v37, v32, v37, s0
	v_and_b32_e32 v38, 0xffff0000, v37
	v_sub_f32_e32 v32, v32, v38
	v_ashrrev_i32_e32 v36, 8, v76
	v_bfe_u32 v38, v32, 16, 1
	v_add3_u32 v32, v32, v38, s0
	v_bitop3_b32 v38, v36, v58, 12 bitop3:0x78
	v_lshl_add_u32 v38, v38, 4, v63
	v_or_b32_e32 v38, v38, v57
	v_add_u32_e32 v39, 0, v38
	ds_write_b16_d16_hi v39, v37
	v_add_u32_e32 v37, s1, v38
	ds_write_b16_d16_hi v37, v32
	v_bfe_u32 v32, v33, 16, 1
	v_add3_u32 v32, v33, v32, s0
	v_and_b32_e32 v37, 0xffff0000, v32
	v_sub_f32_e32 v33, v33, v37
	v_bfe_u32 v37, v33, 16, 1
	v_add3_u32 v33, v33, v37, s0
	v_bitop3_b32 v37, v59, v36, 13 bitop3:0x6c
	v_lshl_add_u32 v37, v37, 4, v67
	v_or_b32_e32 v37, v37, v57
	v_add_u32_e32 v38, 0, v37
	ds_write_b16_d16_hi v38, v32
	v_add_u32_e32 v32, s1, v37
	ds_write_b16_d16_hi v32, v33
	v_bfe_u32 v32, v34, 16, 1
	v_add3_u32 v32, v34, v32, s0
	v_and_b32_e32 v33, 0xffff0000, v32
	v_sub_f32_e32 v33, v34, v33
	v_bfe_u32 v34, v33, 16, 1
	v_add3_u32 v33, v33, v34, s0
	v_bitop3_b32 v34, v61, v36, 14 bitop3:0x6c
	v_lshl_add_u32 v34, v34, 4, v69
	v_or_b32_e32 v34, v34, v57
	v_add_u32_e32 v37, 0, v34
	ds_write_b16_d16_hi v37, v32
	v_add_u32_e32 v32, s1, v34
	ds_write_b16_d16_hi v32, v33
	v_bfe_u32 v32, v35, 16, 1
	v_add3_u32 v32, v35, v32, s0
	v_and_b32_e32 v33, 0xffff0000, v32
	v_sub_f32_e32 v33, v35, v33
	v_bfe_u32 v34, v33, 16, 1
	v_add3_u32 v33, v33, v34, s0
	v_bitop3_b32 v34, v65, v36, 15 bitop3:0x6c
	v_lshl_add_u32 v34, v34, 4, v71
	v_or_b32_e32 v34, v34, v57
	v_add_u32_e32 v35, 0, v34
	ds_write_b16_d16_hi v35, v32
	v_add_u32_e32 v32, s1, v34
	ds_write_b16_d16_hi v32, v33
	s_waitcnt vmcnt(7)
	v_bfe_u32 v33, v28, 16, 1
	v_add3_u32 v33, v28, v33, s0
	v_and_b32_e32 v34, 0xffff0000, v33
	v_sub_f32_e32 v28, v28, v34
	v_ashrrev_i32_e32 v32, 8, v74
	v_bfe_u32 v34, v28, 16, 1
	v_add3_u32 v28, v28, v34, s0
	v_bitop3_b32 v34, v32, v58, 12 bitop3:0x78
	v_lshl_add_u32 v34, v34, 4, v63
	v_or_b32_e32 v34, v34, v57
	v_add_u32_e32 v35, 0, v34
	ds_write_b16_d16_hi v35, v33
	v_add_u32_e32 v33, s1, v34
	ds_write_b16_d16_hi v33, v28
	v_bfe_u32 v28, v29, 16, 1
	v_add3_u32 v28, v29, v28, s0
	v_and_b32_e32 v33, 0xffff0000, v28
	v_sub_f32_e32 v29, v29, v33
	v_bfe_u32 v33, v29, 16, 1
	v_add3_u32 v29, v29, v33, s0
	v_bitop3_b32 v33, v59, v32, 13 bitop3:0x6c
	v_lshl_add_u32 v33, v33, 4, v67
	v_or_b32_e32 v33, v33, v57
	v_add_u32_e32 v34, 0, v33
	ds_write_b16_d16_hi v34, v28
	v_add_u32_e32 v28, s1, v33
	ds_write_b16_d16_hi v28, v29
	v_bfe_u32 v28, v30, 16, 1
	v_add3_u32 v28, v30, v28, s0
	v_and_b32_e32 v29, 0xffff0000, v28
	v_sub_f32_e32 v29, v30, v29
	v_bfe_u32 v30, v29, 16, 1
	v_add3_u32 v29, v29, v30, s0
	v_bitop3_b32 v30, v61, v32, 14 bitop3:0x6c
	v_lshl_add_u32 v30, v30, 4, v69
	v_or_b32_e32 v30, v30, v57
	v_add_u32_e32 v33, 0, v30
	ds_write_b16_d16_hi v33, v28
	v_add_u32_e32 v28, s1, v30
	ds_write_b16_d16_hi v28, v29
	v_bfe_u32 v28, v31, 16, 1
	v_add3_u32 v28, v31, v28, s0
	v_and_b32_e32 v29, 0xffff0000, v28
	v_sub_f32_e32 v29, v31, v29
	v_bfe_u32 v30, v29, 16, 1
	v_add3_u32 v29, v29, v30, s0
	v_bitop3_b32 v30, v65, v32, 15 bitop3:0x6c
	v_lshl_add_u32 v30, v30, 4, v71
	v_or_b32_e32 v30, v30, v57
	v_add_u32_e32 v31, 0, v30
	ds_write_b16_d16_hi v31, v28
	v_add_u32_e32 v28, s1, v30
	ds_write_b16_d16_hi v28, v29
	s_waitcnt vmcnt(6)
	v_bfe_u32 v29, v24, 16, 1
	v_add3_u32 v29, v24, v29, s0
	v_and_b32_e32 v30, 0xffff0000, v29
	v_sub_f32_e32 v24, v24, v30
	v_ashrrev_i32_e32 v28, 8, v72
	v_bfe_u32 v30, v24, 16, 1
	v_add3_u32 v24, v24, v30, s0
	v_bitop3_b32 v30, v28, v58, 12 bitop3:0x78
	v_lshl_add_u32 v30, v30, 4, v63
	v_or_b32_e32 v30, v30, v57
	v_add_u32_e32 v31, 0, v30
	ds_write_b16_d16_hi v31, v29
	v_add_u32_e32 v29, s1, v30
	ds_write_b16_d16_hi v29, v24
	v_bfe_u32 v24, v25, 16, 1
	v_add3_u32 v24, v25, v24, s0
	v_and_b32_e32 v29, 0xffff0000, v24
	v_sub_f32_e32 v25, v25, v29
	v_bfe_u32 v29, v25, 16, 1
	v_add3_u32 v25, v25, v29, s0
	v_bitop3_b32 v29, v59, v28, 13 bitop3:0x6c
	v_lshl_add_u32 v29, v29, 4, v67
	v_or_b32_e32 v29, v29, v57
	v_add_u32_e32 v30, 0, v29
	ds_write_b16_d16_hi v30, v24
	v_add_u32_e32 v24, s1, v29
	ds_write_b16_d16_hi v24, v25
	v_bfe_u32 v24, v26, 16, 1
	v_add3_u32 v24, v26, v24, s0
	v_and_b32_e32 v25, 0xffff0000, v24
	v_sub_f32_e32 v25, v26, v25
	v_bfe_u32 v26, v25, 16, 1
	v_add3_u32 v25, v25, v26, s0
	v_bitop3_b32 v26, v61, v28, 14 bitop3:0x6c
	v_lshl_add_u32 v26, v26, 4, v69
	v_or_b32_e32 v26, v26, v57
	v_add_u32_e32 v29, 0, v26
	ds_write_b16_d16_hi v29, v24
	v_add_u32_e32 v24, s1, v26
	ds_write_b16_d16_hi v24, v25
	v_bfe_u32 v24, v27, 16, 1
	v_add3_u32 v24, v27, v24, s0
	v_and_b32_e32 v25, 0xffff0000, v24
	v_sub_f32_e32 v25, v27, v25
	v_bfe_u32 v26, v25, 16, 1
	v_add3_u32 v25, v25, v26, s0
	v_bitop3_b32 v26, v65, v28, 15 bitop3:0x6c
	v_lshl_add_u32 v26, v26, 4, v71
	v_or_b32_e32 v26, v26, v57
	v_add_u32_e32 v27, 0, v26
	ds_write_b16_d16_hi v27, v24
	v_add_u32_e32 v24, s1, v26
	ds_write_b16_d16_hi v24, v25
	s_waitcnt vmcnt(5)
	v_bfe_u32 v25, v20, 16, 1
	v_add3_u32 v25, v20, v25, s0
	v_and_b32_e32 v26, 0xffff0000, v25
	v_sub_f32_e32 v20, v20, v26
	v_ashrrev_i32_e32 v24, 8, v70
	v_bfe_u32 v26, v20, 16, 1
	v_add3_u32 v20, v20, v26, s0
	v_bitop3_b32 v26, v24, v58, 12 bitop3:0x78
	v_lshl_add_u32 v26, v26, 4, v63
	v_or_b32_e32 v26, v26, v57
	v_add_u32_e32 v27, 0, v26
	ds_write_b16_d16_hi v27, v25
	v_add_u32_e32 v25, s1, v26
	ds_write_b16_d16_hi v25, v20
	v_bfe_u32 v20, v21, 16, 1
	v_add3_u32 v20, v21, v20, s0
	v_and_b32_e32 v25, 0xffff0000, v20
	v_sub_f32_e32 v21, v21, v25
	v_bfe_u32 v25, v21, 16, 1
	v_add3_u32 v21, v21, v25, s0
	v_bitop3_b32 v25, v59, v24, 13 bitop3:0x6c
	v_lshl_add_u32 v25, v25, 4, v67
	v_or_b32_e32 v25, v25, v57
	v_add_u32_e32 v26, 0, v25
	ds_write_b16_d16_hi v26, v20
	v_add_u32_e32 v20, s1, v25
	ds_write_b16_d16_hi v20, v21
	v_bfe_u32 v20, v22, 16, 1
	v_add3_u32 v20, v22, v20, s0
	v_and_b32_e32 v21, 0xffff0000, v20
	v_sub_f32_e32 v21, v22, v21
	v_bfe_u32 v22, v21, 16, 1
	v_add3_u32 v21, v21, v22, s0
	v_bitop3_b32 v22, v61, v24, 14 bitop3:0x6c
	v_lshl_add_u32 v22, v22, 4, v69
	v_or_b32_e32 v22, v22, v57
	v_add_u32_e32 v25, 0, v22
	ds_write_b16_d16_hi v25, v20
	v_add_u32_e32 v20, s1, v22
	ds_write_b16_d16_hi v20, v21
	v_bfe_u32 v20, v23, 16, 1
	v_add3_u32 v20, v23, v20, s0
	v_and_b32_e32 v21, 0xffff0000, v20
	v_sub_f32_e32 v21, v23, v21
	v_bfe_u32 v22, v21, 16, 1
	v_add3_u32 v21, v21, v22, s0
	v_bitop3_b32 v22, v65, v24, 15 bitop3:0x6c
	v_lshl_add_u32 v22, v22, 4, v71
	v_or_b32_e32 v22, v22, v57
	v_add_u32_e32 v23, 0, v22
	ds_write_b16_d16_hi v23, v20
	v_add_u32_e32 v20, s1, v22
	ds_write_b16_d16_hi v20, v21
	s_waitcnt vmcnt(4)
	v_bfe_u32 v21, v16, 16, 1
	v_add3_u32 v21, v16, v21, s0
	v_and_b32_e32 v22, 0xffff0000, v21
	v_sub_f32_e32 v16, v16, v22
	v_ashrrev_i32_e32 v20, 8, v68
	v_bfe_u32 v22, v16, 16, 1
	v_add3_u32 v16, v16, v22, s0
	v_bitop3_b32 v22, v20, v58, 12 bitop3:0x78
	v_lshl_add_u32 v22, v22, 4, v63
	v_or_b32_e32 v22, v22, v57
	v_add_u32_e32 v23, 0, v22
	ds_write_b16_d16_hi v23, v21
	v_add_u32_e32 v21, s1, v22
	ds_write_b16_d16_hi v21, v16
	v_bfe_u32 v16, v17, 16, 1
	v_add3_u32 v16, v17, v16, s0
	v_and_b32_e32 v21, 0xffff0000, v16
	v_sub_f32_e32 v17, v17, v21
	v_bfe_u32 v21, v17, 16, 1
	v_add3_u32 v17, v17, v21, s0
	v_bitop3_b32 v21, v59, v20, 13 bitop3:0x6c
	v_lshl_add_u32 v21, v21, 4, v67
	v_or_b32_e32 v21, v21, v57
	v_add_u32_e32 v22, 0, v21
	ds_write_b16_d16_hi v22, v16
	v_add_u32_e32 v16, s1, v21
	ds_write_b16_d16_hi v16, v17
	v_bfe_u32 v16, v18, 16, 1
	v_add3_u32 v16, v18, v16, s0
	v_and_b32_e32 v17, 0xffff0000, v16
	v_sub_f32_e32 v17, v18, v17
	v_bfe_u32 v18, v17, 16, 1
	v_add3_u32 v17, v17, v18, s0
	v_bitop3_b32 v18, v61, v20, 14 bitop3:0x6c
	v_lshl_add_u32 v18, v18, 4, v69
	v_or_b32_e32 v18, v18, v57
	v_add_u32_e32 v21, 0, v18
	ds_write_b16_d16_hi v21, v16
	v_add_u32_e32 v16, s1, v18
	ds_write_b16_d16_hi v16, v17
	v_bfe_u32 v16, v19, 16, 1
	v_add3_u32 v16, v19, v16, s0
	v_and_b32_e32 v17, 0xffff0000, v16
	v_sub_f32_e32 v17, v19, v17
	v_bfe_u32 v18, v17, 16, 1
	v_add3_u32 v17, v17, v18, s0
	v_bitop3_b32 v18, v65, v20, 15 bitop3:0x6c
	v_lshl_add_u32 v18, v18, 4, v71
	v_or_b32_e32 v18, v18, v57
	v_add_u32_e32 v19, 0, v18
	ds_write_b16_d16_hi v19, v16
	v_add_u32_e32 v16, s1, v18
	ds_write_b16_d16_hi v16, v17
	s_waitcnt vmcnt(3)
	v_bfe_u32 v17, v12, 16, 1
	v_add3_u32 v17, v12, v17, s0
	v_and_b32_e32 v18, 0xffff0000, v17
	v_sub_f32_e32 v12, v12, v18
	v_ashrrev_i32_e32 v16, 8, v66
	v_bfe_u32 v18, v12, 16, 1
	v_add3_u32 v12, v12, v18, s0
	v_bitop3_b32 v18, v16, v58, 12 bitop3:0x78
	v_lshl_add_u32 v18, v18, 4, v63
	v_or_b32_e32 v18, v18, v57
	v_add_u32_e32 v19, 0, v18
	ds_write_b16_d16_hi v19, v17
	v_add_u32_e32 v17, s1, v18
	ds_write_b16_d16_hi v17, v12
	v_bfe_u32 v12, v13, 16, 1
	v_add3_u32 v12, v13, v12, s0
	v_and_b32_e32 v17, 0xffff0000, v12
	v_sub_f32_e32 v13, v13, v17
	v_bfe_u32 v17, v13, 16, 1
	v_add3_u32 v13, v13, v17, s0
	v_bitop3_b32 v17, v59, v16, 13 bitop3:0x6c
	v_lshl_add_u32 v17, v17, 4, v67
	v_or_b32_e32 v17, v17, v57
	v_add_u32_e32 v18, 0, v17
	ds_write_b16_d16_hi v18, v12
	v_add_u32_e32 v12, s1, v17
	ds_write_b16_d16_hi v12, v13
	v_bfe_u32 v12, v14, 16, 1
	v_add3_u32 v12, v14, v12, s0
	v_and_b32_e32 v13, 0xffff0000, v12
	v_sub_f32_e32 v13, v14, v13
	v_bfe_u32 v14, v13, 16, 1
	v_add3_u32 v13, v13, v14, s0
	v_bitop3_b32 v14, v61, v16, 14 bitop3:0x6c
	v_lshl_add_u32 v14, v14, 4, v69
	v_or_b32_e32 v14, v14, v57
	v_add_u32_e32 v17, 0, v14
	ds_write_b16_d16_hi v17, v12
	v_add_u32_e32 v12, s1, v14
	ds_write_b16_d16_hi v12, v13
	v_bfe_u32 v12, v15, 16, 1
	v_add3_u32 v12, v15, v12, s0
	v_and_b32_e32 v13, 0xffff0000, v12
	v_sub_f32_e32 v13, v15, v13
	v_bfe_u32 v14, v13, 16, 1
	v_add3_u32 v13, v13, v14, s0
	v_bitop3_b32 v14, v65, v16, 15 bitop3:0x6c
	v_lshl_add_u32 v14, v14, 4, v71
	v_or_b32_e32 v14, v14, v57
	v_add_u32_e32 v15, 0, v14
	ds_write_b16_d16_hi v15, v12
	v_add_u32_e32 v12, s1, v14
	ds_write_b16_d16_hi v12, v13
	s_waitcnt vmcnt(2)
	v_bfe_u32 v13, v8, 16, 1
	v_add3_u32 v13, v8, v13, s0
	v_and_b32_e32 v14, 0xffff0000, v13
	v_sub_f32_e32 v8, v8, v14
	v_ashrrev_i32_e32 v12, 8, v64
	v_bfe_u32 v14, v8, 16, 1
	v_add3_u32 v8, v8, v14, s0
	v_bitop3_b32 v14, v12, v58, 12 bitop3:0x78
	v_lshl_add_u32 v14, v14, 4, v63
	v_or_b32_e32 v14, v14, v57
	v_add_u32_e32 v15, 0, v14
	ds_write_b16_d16_hi v15, v13
	v_add_u32_e32 v13, s1, v14
	ds_write_b16_d16_hi v13, v8
	v_bfe_u32 v8, v9, 16, 1
	v_add3_u32 v8, v9, v8, s0
	v_and_b32_e32 v13, 0xffff0000, v8
	v_sub_f32_e32 v9, v9, v13
	v_bfe_u32 v13, v9, 16, 1
	v_add3_u32 v9, v9, v13, s0
	v_bitop3_b32 v13, v59, v12, 13 bitop3:0x6c
	v_lshl_add_u32 v13, v13, 4, v67
	v_or_b32_e32 v13, v13, v57
	v_add_u32_e32 v14, 0, v13
	ds_write_b16_d16_hi v14, v8
	v_add_u32_e32 v8, s1, v13
	ds_write_b16_d16_hi v8, v9
	v_bfe_u32 v8, v10, 16, 1
	v_add3_u32 v8, v10, v8, s0
	v_and_b32_e32 v9, 0xffff0000, v8
	v_sub_f32_e32 v9, v10, v9
	v_bfe_u32 v10, v9, 16, 1
	v_add3_u32 v9, v9, v10, s0
	v_bitop3_b32 v10, v61, v12, 14 bitop3:0x6c
	v_lshl_add_u32 v10, v10, 4, v69
	v_or_b32_e32 v10, v10, v57
	v_add_u32_e32 v13, 0, v10
	ds_write_b16_d16_hi v13, v8
	v_add_u32_e32 v8, s1, v10
	ds_write_b16_d16_hi v8, v9
	v_bfe_u32 v8, v11, 16, 1
	v_add3_u32 v8, v11, v8, s0
	v_and_b32_e32 v9, 0xffff0000, v8
	v_sub_f32_e32 v9, v11, v9
	v_bfe_u32 v10, v9, 16, 1
	v_add3_u32 v9, v9, v10, s0
	v_bitop3_b32 v10, v65, v12, 15 bitop3:0x6c
	v_lshl_add_u32 v10, v10, 4, v71
	v_or_b32_e32 v10, v10, v57
	v_add_u32_e32 v11, 0, v10
	ds_write_b16_d16_hi v11, v8
	v_add_u32_e32 v8, s1, v10
	ds_write_b16_d16_hi v8, v9
	s_waitcnt vmcnt(1)
	v_bfe_u32 v9, v4, 16, 1
	v_add3_u32 v9, v4, v9, s0
	v_and_b32_e32 v10, 0xffff0000, v9
	v_sub_f32_e32 v4, v4, v10
	v_ashrrev_i32_e32 v8, 8, v62
	v_bfe_u32 v10, v4, 16, 1
	v_add3_u32 v4, v4, v10, s0
	v_bitop3_b32 v10, v8, v58, 12 bitop3:0x78
	v_lshl_add_u32 v10, v10, 4, v63
	v_or_b32_e32 v10, v10, v57
	v_add_u32_e32 v11, 0, v10
	ds_write_b16_d16_hi v11, v9
	v_add_u32_e32 v9, s1, v10
	ds_write_b16_d16_hi v9, v4
	v_bfe_u32 v4, v5, 16, 1
	v_add3_u32 v4, v5, v4, s0
	v_and_b32_e32 v9, 0xffff0000, v4
	v_sub_f32_e32 v5, v5, v9
	v_bfe_u32 v9, v5, 16, 1
	v_add3_u32 v5, v5, v9, s0
	v_bitop3_b32 v9, v59, v8, 13 bitop3:0x6c
	v_lshl_add_u32 v9, v9, 4, v67
	v_or_b32_e32 v9, v9, v57
	v_add_u32_e32 v10, 0, v9
	ds_write_b16_d16_hi v10, v4
	v_add_u32_e32 v4, s1, v9
	ds_write_b16_d16_hi v4, v5
	v_bfe_u32 v4, v6, 16, 1
	v_add3_u32 v4, v6, v4, s0
	v_and_b32_e32 v5, 0xffff0000, v4
	v_sub_f32_e32 v5, v6, v5
	v_bfe_u32 v6, v5, 16, 1
	v_add3_u32 v5, v5, v6, s0
	v_bitop3_b32 v6, v61, v8, 14 bitop3:0x6c
	v_lshl_add_u32 v6, v6, 4, v69
	v_or_b32_e32 v6, v6, v57
	v_add_u32_e32 v9, 0, v6
	ds_write_b16_d16_hi v9, v4
	v_add_u32_e32 v4, s1, v6
	ds_write_b16_d16_hi v4, v5
	v_bfe_u32 v4, v7, 16, 1
	v_add3_u32 v4, v7, v4, s0
	v_and_b32_e32 v5, 0xffff0000, v4
	v_sub_f32_e32 v5, v7, v5
	v_bfe_u32 v6, v5, 16, 1
	v_add3_u32 v5, v5, v6, s0
	v_bitop3_b32 v6, v65, v8, 15 bitop3:0x6c
	v_lshl_add_u32 v6, v6, 4, v71
	v_or_b32_e32 v6, v6, v57
	v_add_u32_e32 v7, 0, v6
	ds_write_b16_d16_hi v7, v4
	v_add_u32_e32 v4, s1, v6
	ds_write_b16_d16_hi v4, v5
	s_waitcnt vmcnt(0)
	v_bfe_u32 v5, v0, 16, 1
	v_add3_u32 v5, v0, v5, s0
	v_and_b32_e32 v6, 0xffff0000, v5
	v_sub_f32_e32 v0, v0, v6
	v_ashrrev_i32_e32 v4, 8, v60
	v_bfe_u32 v6, v0, 16, 1
	v_add3_u32 v0, v0, v6, s0
	v_bitop3_b32 v6, v4, v58, 12 bitop3:0x78
	v_lshl_add_u32 v6, v6, 4, v63
	v_or_b32_e32 v6, v6, v57
	v_add_u32_e32 v7, 0, v6
	ds_write_b16_d16_hi v7, v5
	v_add_u32_e32 v5, s1, v6
	ds_write_b16_d16_hi v5, v0
	v_bfe_u32 v0, v1, 16, 1
	v_add3_u32 v0, v1, v0, s0
	v_and_b32_e32 v5, 0xffff0000, v0
	v_sub_f32_e32 v1, v1, v5
	v_bfe_u32 v5, v1, 16, 1
	v_add3_u32 v1, v1, v5, s0
	v_bitop3_b32 v5, v59, v4, 13 bitop3:0x6c
	v_lshl_add_u32 v5, v5, 4, v67
	v_or_b32_e32 v5, v5, v57
	v_add_u32_e32 v6, 0, v5
	ds_write_b16_d16_hi v6, v0
	v_add_u32_e32 v0, s1, v5
	ds_write_b16_d16_hi v0, v1
	v_bfe_u32 v0, v2, 16, 1
	v_add3_u32 v0, v2, v0, s0
	v_and_b32_e32 v1, 0xffff0000, v0
	v_sub_f32_e32 v1, v2, v1
	v_bfe_u32 v2, v1, 16, 1
	v_add3_u32 v1, v1, v2, s0
	v_bitop3_b32 v2, v61, v4, 14 bitop3:0x6c
	v_lshl_add_u32 v2, v2, 4, v69
	v_or_b32_e32 v2, v2, v57
	v_add_u32_e32 v5, 0, v2
	ds_write_b16_d16_hi v5, v0
	v_add_u32_e32 v0, s1, v2
	ds_write_b16_d16_hi v0, v1
	v_bfe_u32 v0, v3, 16, 1
	v_add3_u32 v0, v3, v0, s0
	v_and_b32_e32 v1, 0xffff0000, v0
	v_sub_f32_e32 v1, v3, v1
	v_bfe_u32 v2, v1, 16, 1
	v_add3_u32 v1, v1, v2, s0
	v_bitop3_b32 v2, v65, v4, 15 bitop3:0x6c
	v_lshl_add_u32 v2, v2, 4, v71
	s_mul_i32 s60, s18, s4
	v_or_b32_e32 v2, v2, v57
	s_min_i32 s4, s60, 0x8000
	s_movk_i32 s5, 0x800
	v_add_u32_e32 v3, 0, v2
	ds_write_b16_d16_hi v3, v0
	v_add_u32_e32 v0, s1, v2
	s_ashr_i32 s65, s4, 11
	v_cmp_gt_i32_e32 vcc, s5, v56
	ds_write_b16_d16_hi v0, v1
	s_and_saveexec_b64 s[0:1], vcc
	s_cbranch_execz .LBB0_575
	s_add_u32 s4, s52, 0x34800000
	s_addc_u32 s5, s53, 0
	s_add_i32 s6, s60, s18
	s_min_i32 s6, s6, 0x8001
	v_max_i32_e32 v0, 0x600, v56
	s_add_i32 s6, s6, -1
	v_sub_u32_e32 v0, v0, v56
	s_ashr_i32 s12, s6, 11
	s_movk_i32 s6, 0x1ff
	v_add_u32_e32 v1, 0x1ff, v0
	v_cmp_lt_u32_e32 vcc, s6, v1
	s_mov_b64 s[8:9], -1
	v_mov_b32_e32 v0, v56
	s_and_saveexec_b64 s[6:7], vcc
	s_cbranch_execz .LBB0_572
	v_lshrrev_b32_e32 v2, 9, v1
	v_add_u32_e32 v0, -1, v2
	v_add_u32_e32 v57, 0x200, v56
	v_lshrrev_b32_e32 v1, 1, v0
	v_add_u32_e32 v3, 1, v1
	v_cmp_lt_u32_e32 vcc, 5, v0
	v_mov_b32_e32 v10, 0
	v_mov_b64_e32 v[0:1], v[56:57]
	s_and_saveexec_b64 s[8:9], vcc
	s_cbranch_execz .LBB0_566
	s_lshl_b32 s10, s94, 8
	s_add_i32 s10, s10, 0
	v_lshl_add_u32 v0, v92, 2, s10
	v_and_b32_e32 v4, -4, v3
	s_mov_b32 s13, 0
	v_add_u32_e32 v5, 0x20000, v0
	s_mov_b64 s[10:11], 0
	s_movk_i32 s14, 0x400
	v_mov_b32_e32 v6, s12
	v_mov_b32_e32 v7, s65
	v_mov_b32_e32 v8, s12
	v_mov_b32_e32 v9, s65
	s_movk_i32 s15, 0xfbff
	s_movk_i32 s16, 0xf800
	s_movk_i32 s17, 0xf400
	v_mov_b64_e32 v[0:1], v[56:57]

.LBB0_687:
	s_or_b64 exec, exec, s[0:1]
	s_setprio 0
	v_readlane_b32 s4, v243, 7
	v_readlane_b32 s5, v243, 8
	s_load_dwordx4 s[0:3], s[4:5], 0x138
	v_readlane_b32 s60, v243, 10
	v_readlane_b32 s61, v243, 11
	s_waitcnt lgkmcnt(0)
	s_cmp_lt_i32 s1, 7
	s_mov_b64 s[0:1], -1
	s_cbranch_scc0 .LBB0_689
	s_waitcnt vmcnt(0)
	s_barrier
	s_mov_b64 s[0:1], 0

.LBB0_1640:
	s_and_b64 vcc, exec, s[0:1]
	s_cbranch_vccz .LBB0_2262
	v_readlane_b32 s6, v243, 7
	v_readlane_b32 s7, v243, 8
	s_load_dwordx4 s[0:3], s[6:7], 0x138
	s_waitcnt lgkmcnt(0)
	s_mov_b64 s[4:5], s[0:1]
	s_cmp_lt_i32 s4, 14
	s_cselect_b64 s[0:1], -1, 0
	s_cmp_gt_i32 s5, 13
	s_cselect_b64 s[2:3], -1, 0
	s_and_b64 s[0:1], s[0:1], s[2:3]
	s_andn2_b64 vcc, exec, s[0:1]
	s_cbranch_vccnz .LBB0_1822
	s_cmp_ge_u32 s33, 0x100
	s_cbranch_scc0 .Lrt_prio_b
	s_setprio 1
.Lrt_prio_b:
	s_mov_b64 s[4:5], s[6:7]
	s_waitcnt vmcnt(0)
	v_mbcnt_lo_u32_b32 v92, -1, 0
	v_mbcnt_hi_u32_b32 v92, -1, v92
	s_load_dwordx4 s[0:3], s[4:5], 0xe8
	s_load_dword s8, s[6:7], 0x148
	s_add_u32 s6, s6, 0x148
	s_addc_u32 s7, s7, 0
	v_writelane_b32 v242, s6, 41
	s_waitcnt lgkmcnt(0)
	s_add_u32 s0, s0, 0x20000
	s_addc_u32 s1, s1, 0
	v_writelane_b32 v242, s7, 42
	s_abs_i32 s6, s8
	v_cvt_f32_u32_e32 v0, s6
	v_add_u32_e32 v56, s33, v92
	v_lshlrev_b32_e32 v58, 2, v56
	v_ashrrev_i32_e32 v59, 31, v58
	v_rcp_iflag_f32_e32 v0, v0
	s_load_dwordx2 s[52:53], s[4:5], 0x130
	s_waitcnt lgkmcnt(0)
	s_barrier
	v_mul_f32_e32 v0, 0x4f7ffffe, v0
	v_cvt_u32_f32_e32 v0, v0
	v_add_u32_e32 v90, 0x800, v58
	v_ashrrev_i32_e32 v91, 31, v90
	v_readfirstlane_b32 s7, v0
	v_lshl_add_u64 v[0:1], v[58:59], 2, s[0:1]
	global_load_dwordx4 v[86:89], v[0:1], off
	v_lshl_add_u64 v[0:1], v[90:91], 2, s[0:1]
	global_load_dwordx4 v[94:97], v[0:1], off
	v_add_u32_e32 v98, 0x1000, v58
	v_add_u32_e32 v84, 0x1800, v58
	v_ashrrev_i32_e32 v99, 31, v98
	v_ashrrev_i32_e32 v85, 31, v84
	v_add_u32_e32 v82, 0x2000, v58
	v_add_u32_e32 v80, 0x2800, v58
	v_lshl_add_u64 v[0:1], v[98:99], 2, s[0:1]
	v_lshl_add_u64 v[2:3], v[84:85], 2, s[0:1]
	v_ashrrev_i32_e32 v83, 31, v82
	v_ashrrev_i32_e32 v81, 31, v80
	v_add_u32_e32 v78, 0x3000, v58
	v_add_u32_e32 v76, 0x3800, v58
	s_sub_i32 s5, 0, s6
	global_load_dwordx4 v[52:55], v[0:1], off
	global_load_dwordx4 v[48:51], v[2:3], off
	v_lshl_add_u64 v[0:1], v[82:83], 2, s[0:1]
	v_lshl_add_u64 v[2:3], v[80:81], 2, s[0:1]
	v_ashrrev_i32_e32 v79, 31, v78
	v_ashrrev_i32_e32 v77, 31, v76
	v_add_u32_e32 v74, 0x4000, v58
	v_add_u32_e32 v72, 0x4800, v58
	s_mul_i32 s5, s5, s7
	global_load_dwordx4 v[44:47], v[0:1], off
	global_load_dwordx4 v[40:43], v[2:3], off
	v_lshl_add_u64 v[0:1], v[78:79], 2, s[0:1]
	v_lshl_add_u64 v[2:3], v[76:77], 2, s[0:1]
	v_ashrrev_i32_e32 v75, 31, v74
	v_ashrrev_i32_e32 v73, 31, v72
	v_add_u32_e32 v70, 0x5000, v58
	v_add_u32_e32 v68, 0x5800, v58
	s_mul_hi_u32 s5, s7, s5
	global_load_dwordx4 v[36:39], v[0:1], off
	global_load_dwordx4 v[32:35], v[2:3], off
	v_lshl_add_u64 v[0:1], v[74:75], 2, s[0:1]
	v_lshl_add_u64 v[2:3], v[72:73], 2, s[0:1]
	v_ashrrev_i32_e32 v71, 31, v70
	v_ashrrev_i32_e32 v69, 31, v68
	v_add_u32_e32 v66, 0x6000, v58
	v_add_u32_e32 v64, 0x6800, v58
	v_add_u32_e32 v62, 0x7000, v58
	v_add_u32_e32 v60, 0x7800, v58
	s_add_i32 s7, s7, s5
	global_load_dwordx4 v[28:31], v[0:1], off
	global_load_dwordx4 v[24:27], v[2:3], off
	v_lshl_add_u64 v[0:1], v[70:71], 2, s[0:1]
	v_lshl_add_u64 v[2:3], v[68:69], 2, s[0:1]
	v_ashrrev_i32_e32 v67, 31, v66
	v_ashrrev_i32_e32 v65, 31, v64
	v_ashrrev_i32_e32 v63, 31, v62
	v_ashrrev_i32_e32 v61, 31, v60
	s_lshr_b32 s5, s7, 17
	global_load_dwordx4 v[20:23], v[0:1], off
	global_load_dwordx4 v[16:19], v[2:3], off
	v_lshl_add_u64 v[0:1], v[66:67], 2, s[0:1]
	v_lshl_add_u64 v[2:3], v[64:65], 2, s[0:1]
	v_lshl_add_u64 v[100:101], v[62:63], 2, s[0:1]
	v_lshl_add_u64 v[102:103], v[60:61], 2, s[0:1]
	s_movk_i32 s0, 0x7fff
	s_mul_i32 s7, s5, s6
	s_sub_i32 s7, 0x8000, s7
	v_writelane_b32 v242, s8, 43
	s_ashr_i32 s4, s8, 31
	s_add_i32 s8, s5, 1
	s_sub_i32 s9, s7, s6
	s_cmp_ge_u32 s7, s6
	v_and_b32_e32 v65, 28, v58
	v_bfe_i32 v73, v56, 6, 24
	s_cselect_b32 s5, s8, s5
	v_lshrrev_b32_e32 v57, 2, v56
	v_bitop3_b32 v67, v58, v73, 12 bitop3:0x6c
	s_cselect_b32 s7, s9, s7
	s_add_i32 s8, s5, 1
	v_and_b32_e32 v57, 14, v57
	s_cmp_ge_u32 s7, s6
	s_cselect_b32 s5, s8, s5
	s_add_i32 s1, 0, 0x10000
	global_load_dwordx4 v[12:15], v[0:1], off
	global_load_dwordx4 v[8:11], v[2:3], off
	global_load_dwordx4 v[4:7], v[100:101], off
	s_nop 0
	global_load_dwordx4 v[0:3], v[102:103], off
	s_xor_b32 s5, s5, s4
	s_sub_i32 s18, s5, s4
	v_readlane_b32 s4, v243, 0
	v_readlane_b32 s5, v243, 1
	s_waitcnt vmcnt(15)
	v_bfe_u32 v59, v86, 16, 1
	v_add3_u32 v59, v86, v59, s0
	v_and_b32_e32 v61, 0xffff0000, v59
	v_sub_f32_e32 v61, v86, v61
	v_bfe_u32 v63, v61, 16, 1
	v_add3_u32 v61, v61, v63, s0
	v_lshlrev_b32_e32 v63, 11, v65
	v_lshl_add_u32 v67, v67, 4, v63
	v_or_b32_e32 v67, v67, v57
	v_add_u32_e32 v69, 0, v67
	ds_write_b16_d16_hi v69, v59
	v_add_u32_e32 v59, s1, v67
	ds_write_b16_d16_hi v59, v61
	v_bfe_u32 v61, v87, 16, 1
	v_add3_u32 v61, v87, v61, s0
	v_and_b32_e32 v67, 0xffff0000, v61
	v_sub_f32_e32 v67, v87, v67
	v_or_b32_e32 v59, 1, v65
	v_bfe_u32 v69, v67, 16, 1
	v_add3_u32 v69, v67, v69, s0
	v_lshlrev_b32_e32 v67, 11, v59
	v_bitop3_b32 v71, v59, v73, 13 bitop3:0x6c
	v_lshl_add_u32 v71, v71, 4, v67
	v_or_b32_e32 v71, v71, v57
	v_add_u32_e32 v75, 0, v71
	ds_write_b16_d16_hi v75, v61
	v_add_u32_e32 v61, s1, v71
	ds_write_b16_d16_hi v61, v69
	v_bfe_u32 v69, v88, 16, 1
	v_add3_u32 v71, v88, v69, s0
	v_and_b32_e32 v69, 0xffff0000, v71
	v_sub_f32_e32 v69, v88, v69
	v_or_b32_e32 v61, 2, v65
	v_bfe_u32 v75, v69, 16, 1
	v_add3_u32 v75, v69, v75, s0
	v_lshlrev_b32_e32 v69, 11, v61
	v_bitop3_b32 v77, v61, v73, 14 bitop3:0x6c
	v_lshl_add_u32 v77, v77, 4, v69
	v_or_b32_e32 v77, v77, v57
	v_add_u32_e32 v79, 0, v77
	ds_write_b16_d16_hi v79, v71
	v_add_u32_e32 v71, s1, v77
	ds_write_b16_d16_hi v71, v75
	v_bfe_u32 v71, v89, 16, 1
	v_add3_u32 v75, v89, v71, s0
	v_and_b32_e32 v71, 0xffff0000, v75
	v_sub_f32_e32 v71, v89, v71
	v_or_b32_e32 v65, 3, v65
	v_bfe_u32 v77, v71, 16, 1
	v_add3_u32 v77, v71, v77, s0
	v_lshlrev_b32_e32 v71, 11, v65
	v_bitop3_b32 v73, v65, v73, 15 bitop3:0x6c
	v_lshl_add_u32 v73, v73, 4, v71
	v_or_b32_e32 v73, v73, v57
	v_add_u32_e32 v79, 0, v73
	ds_write_b16_d16_hi v79, v75
	s_waitcnt vmcnt(14)
	v_bfe_u32 v75, v94, 16, 1
	v_add_u32_e32 v73, s1, v73
	v_add3_u32 v75, v94, v75, s0
	ds_write_b16_d16_hi v73, v77
	v_and_b32_e32 v77, 0xffff0000, v75
	v_sub_f32_e32 v77, v94, v77
	v_ashrrev_i32_e32 v73, 8, v90
	v_bfe_u32 v79, v77, 16, 1
	v_add3_u32 v77, v77, v79, s0
	v_bitop3_b32 v79, v73, v58, 12 bitop3:0x78
	v_lshl_add_u32 v79, v79, 4, v63
	v_or_b32_e32 v79, v79, v57
	v_add_u32_e32 v81, 0, v79
	ds_write_b16_d16_hi v81, v75
	v_add_u32_e32 v75, s1, v79
	ds_write_b16_d16_hi v75, v77
	v_bfe_u32 v75, v95, 16, 1
	v_add3_u32 v75, v95, v75, s0
	v_and_b32_e32 v77, 0xffff0000, v75
	v_sub_f32_e32 v77, v95, v77
	v_bfe_u32 v79, v77, 16, 1
	v_add3_u32 v77, v77, v79, s0
	v_bitop3_b32 v79, v59, v73, 13 bitop3:0x6c
	v_lshl_add_u32 v79, v79, 4, v67
	v_or_b32_e32 v79, v79, v57
	v_add_u32_e32 v81, 0, v79
	ds_write_b16_d16_hi v81, v75
	v_add_u32_e32 v75, s1, v79
	ds_write_b16_d16_hi v75, v77
	v_bfe_u32 v75, v96, 16, 1
	v_add3_u32 v75, v96, v75, s0
	v_and_b32_e32 v77, 0xffff0000, v75
	v_sub_f32_e32 v77, v96, v77
	v_bfe_u32 v79, v77, 16, 1
	v_add3_u32 v77, v77, v79, s0
	v_bitop3_b32 v79, v61, v73, 14 bitop3:0x6c
	v_lshl_add_u32 v79, v79, 4, v69
	v_or_b32_e32 v79, v79, v57
	v_add_u32_e32 v81, 0, v79
	ds_write_b16_d16_hi v81, v75
	v_add_u32_e32 v75, s1, v79
	ds_write_b16_d16_hi v75, v77
	v_bfe_u32 v75, v97, 16, 1
	v_add3_u32 v75, v97, v75, s0
	v_and_b32_e32 v77, 0xffff0000, v75
	v_bitop3_b32 v73, v65, v73, 15 bitop3:0x6c
	v_sub_f32_e32 v77, v97, v77
	v_lshl_add_u32 v73, v73, 4, v71
	v_bfe_u32 v79, v77, 16, 1
	v_or_b32_e32 v73, v73, v57
	v_add3_u32 v77, v77, v79, s0
	v_add_u32_e32 v79, 0, v73
	ds_write_b16_d16_hi v79, v75
	s_waitcnt vmcnt(13)
	v_bfe_u32 v75, v52, 16, 1
	v_add_u32_e32 v73, s1, v73
	v_add3_u32 v75, v52, v75, s0
	ds_write_b16_d16_hi v73, v77
	v_and_b32_e32 v77, 0xffff0000, v75
	v_sub_f32_e32 v52, v52, v77
	v_ashrrev_i32_e32 v73, 8, v98
	v_bfe_u32 v77, v52, 16, 1
	v_add3_u32 v52, v52, v77, s0
	v_bitop3_b32 v77, v73, v58, 12 bitop3:0x78
	v_lshl_add_u32 v77, v77, 4, v63
	v_or_b32_e32 v77, v77, v57
	v_add_u32_e32 v79, 0, v77
	ds_write_b16_d16_hi v79, v75
	v_add_u32_e32 v75, s1, v77
	ds_write_b16_d16_hi v75, v52
	v_bfe_u32 v52, v53, 16, 1
	v_add3_u32 v52, v53, v52, s0
	v_and_b32_e32 v75, 0xffff0000, v52
	v_sub_f32_e32 v53, v53, v75
	v_bfe_u32 v75, v53, 16, 1
	v_add3_u32 v53, v53, v75, s0
	v_bitop3_b32 v75, v59, v73, 13 bitop3:0x6c
	v_lshl_add_u32 v75, v75, 4, v67
	v_or_b32_e32 v75, v75, v57
	v_add_u32_e32 v77, 0, v75
	ds_write_b16_d16_hi v77, v52
	v_add_u32_e32 v52, s1, v75
	ds_write_b16_d16_hi v52, v53
	v_bfe_u32 v52, v54, 16, 1
	v_add3_u32 v52, v54, v52, s0
	v_and_b32_e32 v53, 0xffff0000, v52
	v_sub_f32_e32 v53, v54, v53
	v_bfe_u32 v54, v53, 16, 1
	v_add3_u32 v53, v53, v54, s0
	v_bitop3_b32 v54, v61, v73, 14 bitop3:0x6c
	v_lshl_add_u32 v54, v54, 4, v69
	v_or_b32_e32 v54, v54, v57
	v_add_u32_e32 v75, 0, v54
	ds_write_b16_d16_hi v75, v52
	v_add_u32_e32 v52, s1, v54
	ds_write_b16_d16_hi v52, v53
	v_bfe_u32 v52, v55, 16, 1
	v_add3_u32 v52, v55, v52, s0
	v_and_b32_e32 v53, 0xffff0000, v52
	v_sub_f32_e32 v53, v55, v53
	v_bfe_u32 v54, v53, 16, 1
	v_add3_u32 v53, v53, v54, s0
	v_bitop3_b32 v54, v65, v73, 15 bitop3:0x6c
	v_lshl_add_u32 v54, v54, 4, v71
	v_or_b32_e32 v54, v54, v57
	v_add_u32_e32 v55, 0, v54
	ds_write_b16_d16_hi v55, v52
	v_add_u32_e32 v52, s1, v54
	ds_write_b16_d16_hi v52, v53
	s_waitcnt vmcnt(12)
	v_bfe_u32 v53, v48, 16, 1
	v_add3_u32 v53, v48, v53, s0
	v_and_b32_e32 v54, 0xffff0000, v53
	v_sub_f32_e32 v48, v48, v54
	v_ashrrev_i32_e32 v52, 8, v84
	v_bfe_u32 v54, v48, 16, 1
	v_add3_u32 v48, v48, v54, s0
	v_bitop3_b32 v54, v52, v58, 12 bitop3:0x78
	v_lshl_add_u32 v54, v54, 4, v63
	v_or_b32_e32 v54, v54, v57
	v_add_u32_e32 v55, 0, v54
	ds_write_b16_d16_hi v55, v53
	v_add_u32_e32 v53, s1, v54
	ds_write_b16_d16_hi v53, v48
	v_bfe_u32 v48, v49, 16, 1
	v_add3_u32 v48, v49, v48, s0
	v_and_b32_e32 v53, 0xffff0000, v48
	v_sub_f32_e32 v49, v49, v53
	v_bfe_u32 v53, v49, 16, 1
	v_add3_u32 v49, v49, v53, s0
	v_bitop3_b32 v53, v59, v52, 13 bitop3:0x6c
	v_lshl_add_u32 v53, v53, 4, v67
	v_or_b32_e32 v53, v53, v57
	v_add_u32_e32 v54, 0, v53
	ds_write_b16_d16_hi v54, v48
	v_add_u32_e32 v48, s1, v53
	ds_write_b16_d16_hi v48, v49
	v_bfe_u32 v48, v50, 16, 1
	v_add3_u32 v48, v50, v48, s0
	v_and_b32_e32 v49, 0xffff0000, v48
	v_sub_f32_e32 v49, v50, v49
	v_bfe_u32 v50, v49, 16, 1
	v_add3_u32 v49, v49, v50, s0
	v_bitop3_b32 v50, v61, v52, 14 bitop3:0x6c
	v_lshl_add_u32 v50, v50, 4, v69
	v_or_b32_e32 v50, v50, v57
	v_add_u32_e32 v53, 0, v50
	ds_write_b16_d16_hi v53, v48
	v_add_u32_e32 v48, s1, v50
	ds_write_b16_d16_hi v48, v49
	v_bfe_u32 v48, v51, 16, 1
	v_add3_u32 v48, v51, v48, s0
	v_and_b32_e32 v49, 0xffff0000, v48
	v_sub_f32_e32 v49, v51, v49
	v_bfe_u32 v50, v49, 16, 1
	v_add3_u32 v49, v49, v50, s0
	v_bitop3_b32 v50, v65, v52, 15 bitop3:0x6c
	v_lshl_add_u32 v50, v50, 4, v71
	v_or_b32_e32 v50, v50, v57
	v_add_u32_e32 v51, 0, v50
	ds_write_b16_d16_hi v51, v48
	v_add_u32_e32 v48, s1, v50
	ds_write_b16_d16_hi v48, v49
	s_waitcnt vmcnt(11)
	v_bfe_u32 v49, v44, 16, 1
	v_add3_u32 v49, v44, v49, s0
	v_and_b32_e32 v50, 0xffff0000, v49
	v_sub_f32_e32 v44, v44, v50
	v_ashrrev_i32_e32 v48, 8, v82
	v_bfe_u32 v50, v44, 16, 1
	v_add3_u32 v44, v44, v50, s0
	v_bitop3_b32 v50, v48, v58, 12 bitop3:0x78
	v_lshl_add_u32 v50, v50, 4, v63
	v_or_b32_e32 v50, v50, v57
	v_add_u32_e32 v51, 0, v50
	ds_write_b16_d16_hi v51, v49
	v_add_u32_e32 v49, s1, v50
	ds_write_b16_d16_hi v49, v44
	v_bfe_u32 v44, v45, 16, 1
	v_add3_u32 v44, v45, v44, s0
	v_and_b32_e32 v49, 0xffff0000, v44
	v_sub_f32_e32 v45, v45, v49
	v_bfe_u32 v49, v45, 16, 1
	v_add3_u32 v45, v45, v49, s0
	v_bitop3_b32 v49, v59, v48, 13 bitop3:0x6c
	v_lshl_add_u32 v49, v49, 4, v67
	v_or_b32_e32 v49, v49, v57
	v_add_u32_e32 v50, 0, v49
	ds_write_b16_d16_hi v50, v44
	v_add_u32_e32 v44, s1, v49
	ds_write_b16_d16_hi v44, v45
	v_bfe_u32 v44, v46, 16, 1
	v_add3_u32 v44, v46, v44, s0
	v_and_b32_e32 v45, 0xffff0000, v44
	v_sub_f32_e32 v45, v46, v45
	v_bfe_u32 v46, v45, 16, 1
	v_add3_u32 v45, v45, v46, s0
	v_bitop3_b32 v46, v61, v48, 14 bitop3:0x6c
	v_lshl_add_u32 v46, v46, 4, v69
	v_or_b32_e32 v46, v46, v57
	v_add_u32_e32 v49, 0, v46
	ds_write_b16_d16_hi v49, v44
	v_add_u32_e32 v44, s1, v46
	ds_write_b16_d16_hi v44, v45
	v_bfe_u32 v44, v47, 16, 1
	v_add3_u32 v44, v47, v44, s0
	v_and_b32_e32 v45, 0xffff0000, v44
	v_sub_f32_e32 v45, v47, v45
	v_bfe_u32 v46, v45, 16, 1
	v_add3_u32 v45, v45, v46, s0
	v_bitop3_b32 v46, v65, v48, 15 bitop3:0x6c
	v_lshl_add_u32 v46, v46, 4, v71
	v_or_b32_e32 v46, v46, v57
	v_add_u32_e32 v47, 0, v46
	ds_write_b16_d16_hi v47, v44
	v_add_u32_e32 v44, s1, v46
	ds_write_b16_d16_hi v44, v45
	s_waitcnt vmcnt(10)
	v_bfe_u32 v45, v40, 16, 1
	v_add3_u32 v45, v40, v45, s0
	v_and_b32_e32 v46, 0xffff0000, v45
	v_sub_f32_e32 v40, v40, v46
	v_ashrrev_i32_e32 v44, 8, v80
	v_bfe_u32 v46, v40, 16, 1
	v_add3_u32 v40, v40, v46, s0
	v_bitop3_b32 v46, v44, v58, 12 bitop3:0x78
	v_lshl_add_u32 v46, v46, 4, v63
	v_or_b32_e32 v46, v46, v57
	v_add_u32_e32 v47, 0, v46
	ds_write_b16_d16_hi v47, v45
	v_add_u32_e32 v45, s1, v46
	ds_write_b16_d16_hi v45, v40
	v_bfe_u32 v40, v41, 16, 1
	v_add3_u32 v40, v41, v40, s0
	v_and_b32_e32 v45, 0xffff0000, v40
	v_sub_f32_e32 v41, v41, v45
	v_bfe_u32 v45, v41, 16, 1
	v_add3_u32 v41, v41, v45, s0
	v_bitop3_b32 v45, v59, v44, 13 bitop3:0x6c
	v_lshl_add_u32 v45, v45, 4, v67
	v_or_b32_e32 v45, v45, v57
	v_add_u32_e32 v46, 0, v45
	ds_write_b16_d16_hi v46, v40
	v_add_u32_e32 v40, s1, v45
	ds_write_b16_d16_hi v40, v41
	v_bfe_u32 v40, v42, 16, 1
	v_add3_u32 v40, v42, v40, s0
	v_and_b32_e32 v41, 0xffff0000, v40
	v_sub_f32_e32 v41, v42, v41
	v_bfe_u32 v42, v41, 16, 1
	v_add3_u32 v41, v41, v42, s0
	v_bitop3_b32 v42, v61, v44, 14 bitop3:0x6c
	v_lshl_add_u32 v42, v42, 4, v69
	v_or_b32_e32 v42, v42, v57
	v_add_u32_e32 v45, 0, v42
	ds_write_b16_d16_hi v45, v40
	v_add_u32_e32 v40, s1, v42
	ds_write_b16_d16_hi v40, v41
	v_bfe_u32 v40, v43, 16, 1
	v_add3_u32 v40, v43, v40, s0
	v_and_b32_e32 v41, 0xffff0000, v40
	v_sub_f32_e32 v41, v43, v41
	v_bfe_u32 v42, v41, 16, 1
	v_add3_u32 v41, v41, v42, s0
	v_bitop3_b32 v42, v65, v44, 15 bitop3:0x6c
	v_lshl_add_u32 v42, v42, 4, v71
	v_or_b32_e32 v42, v42, v57
	v_add_u32_e32 v43, 0, v42
	ds_write_b16_d16_hi v43, v40
	v_add_u32_e32 v40, s1, v42
	ds_write_b16_d16_hi v40, v41
	s_waitcnt vmcnt(9)
	v_bfe_u32 v41, v36, 16, 1
	v_add3_u32 v41, v36, v41, s0
	v_and_b32_e32 v42, 0xffff0000, v41
	v_sub_f32_e32 v36, v36, v42
	v_ashrrev_i32_e32 v40, 8, v78
	v_bfe_u32 v42, v36, 16, 1
	v_add3_u32 v36, v36, v42, s0
	v_bitop3_b32 v42, v40, v58, 12 bitop3:0x78
	v_lshl_add_u32 v42, v42, 4, v63
	v_or_b32_e32 v42, v42, v57
	v_add_u32_e32 v43, 0, v42
	ds_write_b16_d16_hi v43, v41
	v_add_u32_e32 v41, s1, v42
	ds_write_b16_d16_hi v41, v36
	v_bfe_u32 v36, v37, 16, 1
	v_add3_u32 v36, v37, v36, s0
	v_and_b32_e32 v41, 0xffff0000, v36
	v_sub_f32_e32 v37, v37, v41
	v_bfe_u32 v41, v37, 16, 1
	v_add3_u32 v37, v37, v41, s0
	v_bitop3_b32 v41, v59, v40, 13 bitop3:0x6c
	v_lshl_add_u32 v41, v41, 4, v67
	v_or_b32_e32 v41, v41, v57
	v_add_u32_e32 v42, 0, v41
	ds_write_b16_d16_hi v42, v36
	v_add_u32_e32 v36, s1, v41
	ds_write_b16_d16_hi v36, v37
	v_bfe_u32 v36, v38, 16, 1
	v_add3_u32 v36, v38, v36, s0
	v_and_b32_e32 v37, 0xffff0000, v36
	v_sub_f32_e32 v37, v38, v37
	v_bfe_u32 v38, v37, 16, 1
	v_add3_u32 v37, v37, v38, s0
	v_bitop3_b32 v38, v61, v40, 14 bitop3:0x6c
	v_lshl_add_u32 v38, v38, 4, v69
	v_or_b32_e32 v38, v38, v57
	v_add_u32_e32 v41, 0, v38
	ds_write_b16_d16_hi v41, v36
	v_add_u32_e32 v36, s1, v38
	ds_write_b16_d16_hi v36, v37
	v_bfe_u32 v36, v39, 16, 1
	v_add3_u32 v36, v39, v36, s0
	v_and_b32_e32 v37, 0xffff0000, v36
	v_sub_f32_e32 v37, v39, v37
	v_bfe_u32 v38, v37, 16, 1
	v_add3_u32 v37, v37, v38, s0
	v_bitop3_b32 v38, v65, v40, 15 bitop3:0x6c
	v_lshl_add_u32 v38, v38, 4, v71
	v_or_b32_e32 v38, v38, v57
	v_add_u32_e32 v39, 0, v38
	ds_write_b16_d16_hi v39, v36
	v_add_u32_e32 v36, s1, v38
	ds_write_b16_d16_hi v36, v37
	s_waitcnt vmcnt(8)
	v_bfe_u32 v37, v32, 16, 1
	v_add3_u32 v37, v32, v37, s0
	v_and_b32_e32 v38, 0xffff0000, v37
	v_sub_f32_e32 v32, v32, v38
	v_ashrrev_i32_e32 v36, 8, v76
	v_bfe_u32 v38, v32, 16, 1
	v_add3_u32 v32, v32, v38, s0
	v_bitop3_b32 v38, v36, v58, 12 bitop3:0x78
	v_lshl_add_u32 v38, v38, 4, v63
	v_or_b32_e32 v38, v38, v57
	v_add_u32_e32 v39, 0, v38
	ds_write_b16_d16_hi v39, v37
	v_add_u32_e32 v37, s1, v38
	ds_write_b16_d16_hi v37, v32
	v_bfe_u32 v32, v33, 16, 1
	v_add3_u32 v32, v33, v32, s0
	v_and_b32_e32 v37, 0xffff0000, v32
	v_sub_f32_e32 v33, v33, v37
	v_bfe_u32 v37, v33, 16, 1
	v_add3_u32 v33, v33, v37, s0
	v_bitop3_b32 v37, v59, v36, 13 bitop3:0x6c
	v_lshl_add_u32 v37, v37, 4, v67
	v_or_b32_e32 v37, v37, v57
	v_add_u32_e32 v38, 0, v37
	ds_write_b16_d16_hi v38, v32
	v_add_u32_e32 v32, s1, v37
	ds_write_b16_d16_hi v32, v33
	v_bfe_u32 v32, v34, 16, 1
	v_add3_u32 v32, v34, v32, s0
	v_and_b32_e32 v33, 0xffff0000, v32
	v_sub_f32_e32 v33, v34, v33
	v_bfe_u32 v34, v33, 16, 1
	v_add3_u32 v33, v33, v34, s0
	v_bitop3_b32 v34, v61, v36, 14 bitop3:0x6c
	v_lshl_add_u32 v34, v34, 4, v69
	v_or_b32_e32 v34, v34, v57
	v_add_u32_e32 v37, 0, v34
	ds_write_b16_d16_hi v37, v32
	v_add_u32_e32 v32, s1, v34
	ds_write_b16_d16_hi v32, v33
	v_bfe_u32 v32, v35, 16, 1
	v_add3_u32 v32, v35, v32, s0
	v_and_b32_e32 v33, 0xffff0000, v32
	v_sub_f32_e32 v33, v35, v33
	v_bfe_u32 v34, v33, 16, 1
	v_add3_u32 v33, v33, v34, s0
	v_bitop3_b32 v34, v65, v36, 15 bitop3:0x6c
	v_lshl_add_u32 v34, v34, 4, v71
	v_or_b32_e32 v34, v34, v57
	v_add_u32_e32 v35, 0, v34
	ds_write_b16_d16_hi v35, v32
	v_add_u32_e32 v32, s1, v34
	ds_write_b16_d16_hi v32, v33
	s_waitcnt vmcnt(7)
	v_bfe_u32 v33, v28, 16, 1
	v_add3_u32 v33, v28, v33, s0
	v_and_b32_e32 v34, 0xffff0000, v33
	v_sub_f32_e32 v28, v28, v34
	v_ashrrev_i32_e32 v32, 8, v74
	v_bfe_u32 v34, v28, 16, 1
	v_add3_u32 v28, v28, v34, s0
	v_bitop3_b32 v34, v32, v58, 12 bitop3:0x78
	v_lshl_add_u32 v34, v34, 4, v63
	v_or_b32_e32 v34, v34, v57
	v_add_u32_e32 v35, 0, v34
	ds_write_b16_d16_hi v35, v33
	v_add_u32_e32 v33, s1, v34
	ds_write_b16_d16_hi v33, v28
	v_bfe_u32 v28, v29, 16, 1
	v_add3_u32 v28, v29, v28, s0
	v_and_b32_e32 v33, 0xffff0000, v28
	v_sub_f32_e32 v29, v29, v33
	v_bfe_u32 v33, v29, 16, 1
	v_add3_u32 v29, v29, v33, s0
	v_bitop3_b32 v33, v59, v32, 13 bitop3:0x6c
	v_lshl_add_u32 v33, v33, 4, v67
	v_or_b32_e32 v33, v33, v57
	v_add_u32_e32 v34, 0, v33
	ds_write_b16_d16_hi v34, v28
	v_add_u32_e32 v28, s1, v33
	ds_write_b16_d16_hi v28, v29
	v_bfe_u32 v28, v30, 16, 1
	v_add3_u32 v28, v30, v28, s0
	v_and_b32_e32 v29, 0xffff0000, v28
	v_sub_f32_e32 v29, v30, v29
	v_bfe_u32 v30, v29, 16, 1
	v_add3_u32 v29, v29, v30, s0
	v_bitop3_b32 v30, v61, v32, 14 bitop3:0x6c
	v_lshl_add_u32 v30, v30, 4, v69
	v_or_b32_e32 v30, v30, v57
	v_add_u32_e32 v33, 0, v30
	ds_write_b16_d16_hi v33, v28
	v_add_u32_e32 v28, s1, v30
	ds_write_b16_d16_hi v28, v29
	v_bfe_u32 v28, v31, 16, 1
	v_add3_u32 v28, v31, v28, s0
	v_and_b32_e32 v29, 0xffff0000, v28
	v_sub_f32_e32 v29, v31, v29
	v_bfe_u32 v30, v29, 16, 1
	v_add3_u32 v29, v29, v30, s0
	v_bitop3_b32 v30, v65, v32, 15 bitop3:0x6c
	v_lshl_add_u32 v30, v30, 4, v71
	v_or_b32_e32 v30, v30, v57
	v_add_u32_e32 v31, 0, v30
	ds_write_b16_d16_hi v31, v28
	v_add_u32_e32 v28, s1, v30
	ds_write_b16_d16_hi v28, v29
	s_waitcnt vmcnt(6)
	v_bfe_u32 v29, v24, 16, 1
	v_add3_u32 v29, v24, v29, s0
	v_and_b32_e32 v30, 0xffff0000, v29
	v_sub_f32_e32 v24, v24, v30
	v_ashrrev_i32_e32 v28, 8, v72
	v_bfe_u32 v30, v24, 16, 1
	v_add3_u32 v24, v24, v30, s0
	v_bitop3_b32 v30, v28, v58, 12 bitop3:0x78
	v_lshl_add_u32 v30, v30, 4, v63
	v_or_b32_e32 v30, v30, v57
	v_add_u32_e32 v31, 0, v30
	ds_write_b16_d16_hi v31, v29
	v_add_u32_e32 v29, s1, v30
	ds_write_b16_d16_hi v29, v24
	v_bfe_u32 v24, v25, 16, 1
	v_add3_u32 v24, v25, v24, s0
	v_and_b32_e32 v29, 0xffff0000, v24
	v_sub_f32_e32 v25, v25, v29
	v_bfe_u32 v29, v25, 16, 1
	v_add3_u32 v25, v25, v29, s0
	v_bitop3_b32 v29, v59, v28, 13 bitop3:0x6c
	v_lshl_add_u32 v29, v29, 4, v67
	v_or_b32_e32 v29, v29, v57
	v_add_u32_e32 v30, 0, v29
	ds_write_b16_d16_hi v30, v24
	v_add_u32_e32 v24, s1, v29
	ds_write_b16_d16_hi v24, v25
	v_bfe_u32 v24, v26, 16, 1
	v_add3_u32 v24, v26, v24, s0
	v_and_b32_e32 v25, 0xffff0000, v24
	v_sub_f32_e32 v25, v26, v25
	v_bfe_u32 v26, v25, 16, 1
	v_add3_u32 v25, v25, v26, s0
	v_bitop3_b32 v26, v61, v28, 14 bitop3:0x6c
	v_lshl_add_u32 v26, v26, 4, v69
	v_or_b32_e32 v26, v26, v57
	v_add_u32_e32 v29, 0, v26
	ds_write_b16_d16_hi v29, v24
	v_add_u32_e32 v24, s1, v26
	ds_write_b16_d16_hi v24, v25
	v_bfe_u32 v24, v27, 16, 1
	v_add3_u32 v24, v27, v24, s0
	v_and_b32_e32 v25, 0xffff0000, v24
	v_sub_f32_e32 v25, v27, v25
	v_bfe_u32 v26, v25, 16, 1
	v_add3_u32 v25, v25, v26, s0
	v_bitop3_b32 v26, v65, v28, 15 bitop3:0x6c
	v_lshl_add_u32 v26, v26, 4, v71
	v_or_b32_e32 v26, v26, v57
	v_add_u32_e32 v27, 0, v26
	ds_write_b16_d16_hi v27, v24
	v_add_u32_e32 v24, s1, v26
	ds_write_b16_d16_hi v24, v25
	s_waitcnt vmcnt(5)
	v_bfe_u32 v25, v20, 16, 1
	v_add3_u32 v25, v20, v25, s0
	v_and_b32_e32 v26, 0xffff0000, v25
	v_sub_f32_e32 v20, v20, v26
	v_ashrrev_i32_e32 v24, 8, v70
	v_bfe_u32 v26, v20, 16, 1
	v_add3_u32 v20, v20, v26, s0
	v_bitop3_b32 v26, v24, v58, 12 bitop3:0x78
	v_lshl_add_u32 v26, v26, 4, v63
	v_or_b32_e32 v26, v26, v57
	v_add_u32_e32 v27, 0, v26
	ds_write_b16_d16_hi v27, v25
	v_add_u32_e32 v25, s1, v26
	ds_write_b16_d16_hi v25, v20
	v_bfe_u32 v20, v21, 16, 1
	v_add3_u32 v20, v21, v20, s0
	v_and_b32_e32 v25, 0xffff0000, v20
	v_sub_f32_e32 v21, v21, v25
	v_bfe_u32 v25, v21, 16, 1
	v_add3_u32 v21, v21, v25, s0
	v_bitop3_b32 v25, v59, v24, 13 bitop3:0x6c
	v_lshl_add_u32 v25, v25, 4, v67
	v_or_b32_e32 v25, v25, v57
	v_add_u32_e32 v26, 0, v25
	ds_write_b16_d16_hi v26, v20
	v_add_u32_e32 v20, s1, v25
	ds_write_b16_d16_hi v20, v21
	v_bfe_u32 v20, v22, 16, 1
	v_add3_u32 v20, v22, v20, s0
	v_and_b32_e32 v21, 0xffff0000, v20
	v_sub_f32_e32 v21, v22, v21
	v_bfe_u32 v22, v21, 16, 1
	v_add3_u32 v21, v21, v22, s0
	v_bitop3_b32 v22, v61, v24, 14 bitop3:0x6c
	v_lshl_add_u32 v22, v22, 4, v69
	v_or_b32_e32 v22, v22, v57
	v_add_u32_e32 v25, 0, v22
	ds_write_b16_d16_hi v25, v20
	v_add_u32_e32 v20, s1, v22
	ds_write_b16_d16_hi v20, v21
	v_bfe_u32 v20, v23, 16, 1
	v_add3_u32 v20, v23, v20, s0
	v_and_b32_e32 v21, 0xffff0000, v20
	v_sub_f32_e32 v21, v23, v21
	v_bfe_u32 v22, v21, 16, 1
	v_add3_u32 v21, v21, v22, s0
	v_bitop3_b32 v22, v65, v24, 15 bitop3:0x6c
	v_lshl_add_u32 v22, v22, 4, v71
	v_or_b32_e32 v22, v22, v57
	v_add_u32_e32 v23, 0, v22
	ds_write_b16_d16_hi v23, v20
	v_add_u32_e32 v20, s1, v22
	ds_write_b16_d16_hi v20, v21
	s_waitcnt vmcnt(4)
	v_bfe_u32 v21, v16, 16, 1
	v_add3_u32 v21, v16, v21, s0
	v_and_b32_e32 v22, 0xffff0000, v21
	v_sub_f32_e32 v16, v16, v22
	v_ashrrev_i32_e32 v20, 8, v68
	v_bfe_u32 v22, v16, 16, 1
	v_add3_u32 v16, v16, v22, s0
	v_bitop3_b32 v22, v20, v58, 12 bitop3:0x78
	v_lshl_add_u32 v22, v22, 4, v63
	v_or_b32_e32 v22, v22, v57
	v_add_u32_e32 v23, 0, v22
	ds_write_b16_d16_hi v23, v21
	v_add_u32_e32 v21, s1, v22
	ds_write_b16_d16_hi v21, v16
	v_bfe_u32 v16, v17, 16, 1
	v_add3_u32 v16, v17, v16, s0
	v_and_b32_e32 v21, 0xffff0000, v16
	v_sub_f32_e32 v17, v17, v21
	v_bfe_u32 v21, v17, 16, 1
	v_add3_u32 v17, v17, v21, s0
	v_bitop3_b32 v21, v59, v20, 13 bitop3:0x6c
	v_lshl_add_u32 v21, v21, 4, v67
	v_or_b32_e32 v21, v21, v57
	v_add_u32_e32 v22, 0, v21
	ds_write_b16_d16_hi v22, v16
	v_add_u32_e32 v16, s1, v21
	ds_write_b16_d16_hi v16, v17
	v_bfe_u32 v16, v18, 16, 1
	v_add3_u32 v16, v18, v16, s0
	v_and_b32_e32 v17, 0xffff0000, v16
	v_sub_f32_e32 v17, v18, v17
	v_bfe_u32 v18, v17, 16, 1
	v_add3_u32 v17, v17, v18, s0
	v_bitop3_b32 v18, v61, v20, 14 bitop3:0x6c
	v_lshl_add_u32 v18, v18, 4, v69
	v_or_b32_e32 v18, v18, v57
	v_add_u32_e32 v21, 0, v18
	ds_write_b16_d16_hi v21, v16
	v_add_u32_e32 v16, s1, v18
	ds_write_b16_d16_hi v16, v17
	v_bfe_u32 v16, v19, 16, 1
	v_add3_u32 v16, v19, v16, s0
	v_and_b32_e32 v17, 0xffff0000, v16
	v_sub_f32_e32 v17, v19, v17
	v_bfe_u32 v18, v17, 16, 1
	v_add3_u32 v17, v17, v18, s0
	v_bitop3_b32 v18, v65, v20, 15 bitop3:0x6c
	v_lshl_add_u32 v18, v18, 4, v71
	v_or_b32_e32 v18, v18, v57
	v_add_u32_e32 v19, 0, v18
	ds_write_b16_d16_hi v19, v16
	v_add_u32_e32 v16, s1, v18
	ds_write_b16_d16_hi v16, v17
	s_waitcnt vmcnt(3)
	v_bfe_u32 v17, v12, 16, 1
	v_add3_u32 v17, v12, v17, s0
	v_and_b32_e32 v18, 0xffff0000, v17
	v_sub_f32_e32 v12, v12, v18
	v_ashrrev_i32_e32 v16, 8, v66
	v_bfe_u32 v18, v12, 16, 1
	v_add3_u32 v12, v12, v18, s0
	v_bitop3_b32 v18, v16, v58, 12 bitop3:0x78
	v_lshl_add_u32 v18, v18, 4, v63
	v_or_b32_e32 v18, v18, v57
	v_add_u32_e32 v19, 0, v18
	ds_write_b16_d16_hi v19, v17
	v_add_u32_e32 v17, s1, v18
	ds_write_b16_d16_hi v17, v12
	v_bfe_u32 v12, v13, 16, 1
	v_add3_u32 v12, v13, v12, s0
	v_and_b32_e32 v17, 0xffff0000, v12
	v_sub_f32_e32 v13, v13, v17
	v_bfe_u32 v17, v13, 16, 1
	v_add3_u32 v13, v13, v17, s0
	v_bitop3_b32 v17, v59, v16, 13 bitop3:0x6c
	v_lshl_add_u32 v17, v17, 4, v67
	v_or_b32_e32 v17, v17, v57
	v_add_u32_e32 v18, 0, v17
	ds_write_b16_d16_hi v18, v12
	v_add_u32_e32 v12, s1, v17
	ds_write_b16_d16_hi v12, v13
	v_bfe_u32 v12, v14, 16, 1
	v_add3_u32 v12, v14, v12, s0
	v_and_b32_e32 v13, 0xffff0000, v12
	v_sub_f32_e32 v13, v14, v13
	v_bfe_u32 v14, v13, 16, 1
	v_add3_u32 v13, v13, v14, s0
	v_bitop3_b32 v14, v61, v16, 14 bitop3:0x6c
	v_lshl_add_u32 v14, v14, 4, v69
	v_or_b32_e32 v14, v14, v57
	v_add_u32_e32 v17, 0, v14
	ds_write_b16_d16_hi v17, v12
	v_add_u32_e32 v12, s1, v14
	ds_write_b16_d16_hi v12, v13
	v_bfe_u32 v12, v15, 16, 1
	v_add3_u32 v12, v15, v12, s0
	v_and_b32_e32 v13, 0xffff0000, v12
	v_sub_f32_e32 v13, v15, v13
	v_bfe_u32 v14, v13, 16, 1
	v_add3_u32 v13, v13, v14, s0
	v_bitop3_b32 v14, v65, v16, 15 bitop3:0x6c
	v_lshl_add_u32 v14, v14, 4, v71
	v_or_b32_e32 v14, v14, v57
	v_add_u32_e32 v15, 0, v14
	ds_write_b16_d16_hi v15, v12
	v_add_u32_e32 v12, s1, v14
	ds_write_b16_d16_hi v12, v13
	s_waitcnt vmcnt(2)
	v_bfe_u32 v13, v8, 16, 1
	v_add3_u32 v13, v8, v13, s0
	v_and_b32_e32 v14, 0xffff0000, v13
	v_sub_f32_e32 v8, v8, v14
	v_ashrrev_i32_e32 v12, 8, v64
	v_bfe_u32 v14, v8, 16, 1
	v_add3_u32 v8, v8, v14, s0
	v_bitop3_b32 v14, v12, v58, 12 bitop3:0x78
	v_lshl_add_u32 v14, v14, 4, v63
	v_or_b32_e32 v14, v14, v57
	v_add_u32_e32 v15, 0, v14
	ds_write_b16_d16_hi v15, v13
	v_add_u32_e32 v13, s1, v14
	ds_write_b16_d16_hi v13, v8
	v_bfe_u32 v8, v9, 16, 1
	v_add3_u32 v8, v9, v8, s0
	v_and_b32_e32 v13, 0xffff0000, v8
	v_sub_f32_e32 v9, v9, v13
	v_bfe_u32 v13, v9, 16, 1
	v_add3_u32 v9, v9, v13, s0
	v_bitop3_b32 v13, v59, v12, 13 bitop3:0x6c
	v_lshl_add_u32 v13, v13, 4, v67
	v_or_b32_e32 v13, v13, v57
	v_add_u32_e32 v14, 0, v13
	ds_write_b16_d16_hi v14, v8
	v_add_u32_e32 v8, s1, v13
	ds_write_b16_d16_hi v8, v9
	v_bfe_u32 v8, v10, 16, 1
	v_add3_u32 v8, v10, v8, s0
	v_and_b32_e32 v9, 0xffff0000, v8
	v_sub_f32_e32 v9, v10, v9
	v_bfe_u32 v10, v9, 16, 1
	v_add3_u32 v9, v9, v10, s0
	v_bitop3_b32 v10, v61, v12, 14 bitop3:0x6c
	v_lshl_add_u32 v10, v10, 4, v69
	v_or_b32_e32 v10, v10, v57
	v_add_u32_e32 v13, 0, v10
	ds_write_b16_d16_hi v13, v8
	v_add_u32_e32 v8, s1, v10
	ds_write_b16_d16_hi v8, v9
	v_bfe_u32 v8, v11, 16, 1
	v_add3_u32 v8, v11, v8, s0
	v_and_b32_e32 v9, 0xffff0000, v8
	v_sub_f32_e32 v9, v11, v9
	v_bfe_u32 v10, v9, 16, 1
	v_add3_u32 v9, v9, v10, s0
	v_bitop3_b32 v10, v65, v12, 15 bitop3:0x6c
	v_lshl_add_u32 v10, v10, 4, v71
	v_or_b32_e32 v10, v10, v57
	v_add_u32_e32 v11, 0, v10
	ds_write_b16_d16_hi v11, v8
	v_add_u32_e32 v8, s1, v10
	ds_write_b16_d16_hi v8, v9
	s_waitcnt vmcnt(1)
	v_bfe_u32 v9, v4, 16, 1
	v_add3_u32 v9, v4, v9, s0
	v_and_b32_e32 v10, 0xffff0000, v9
	v_sub_f32_e32 v4, v4, v10
	v_ashrrev_i32_e32 v8, 8, v62
	v_bfe_u32 v10, v4, 16, 1
	v_add3_u32 v4, v4, v10, s0
	v_bitop3_b32 v10, v8, v58, 12 bitop3:0x78
	v_lshl_add_u32 v10, v10, 4, v63
	v_or_b32_e32 v10, v10, v57
	v_add_u32_e32 v11, 0, v10
	ds_write_b16_d16_hi v11, v9
	v_add_u32_e32 v9, s1, v10
	ds_write_b16_d16_hi v9, v4
	v_bfe_u32 v4, v5, 16, 1
	v_add3_u32 v4, v5, v4, s0
	v_and_b32_e32 v9, 0xffff0000, v4
	v_sub_f32_e32 v5, v5, v9
	v_bfe_u32 v9, v5, 16, 1
	v_add3_u32 v5, v5, v9, s0
	v_bitop3_b32 v9, v59, v8, 13 bitop3:0x6c
	v_lshl_add_u32 v9, v9, 4, v67
	v_or_b32_e32 v9, v9, v57
	v_add_u32_e32 v10, 0, v9
	ds_write_b16_d16_hi v10, v4
	v_add_u32_e32 v4, s1, v9
	ds_write_b16_d16_hi v4, v5
	v_bfe_u32 v4, v6, 16, 1
	v_add3_u32 v4, v6, v4, s0
	v_and_b32_e32 v5, 0xffff0000, v4
	v_sub_f32_e32 v5, v6, v5
	v_bfe_u32 v6, v5, 16, 1
	v_add3_u32 v5, v5, v6, s0
	v_bitop3_b32 v6, v61, v8, 14 bitop3:0x6c
	v_lshl_add_u32 v6, v6, 4, v69
	v_or_b32_e32 v6, v6, v57
	v_add_u32_e32 v9, 0, v6
	ds_write_b16_d16_hi v9, v4
	v_add_u32_e32 v4, s1, v6
	ds_write_b16_d16_hi v4, v5
	v_bfe_u32 v4, v7, 16, 1
	v_add3_u32 v4, v7, v4, s0
	v_and_b32_e32 v5, 0xffff0000, v4
	v_sub_f32_e32 v5, v7, v5
	v_bfe_u32 v6, v5, 16, 1
	v_add3_u32 v5, v5, v6, s0
	v_bitop3_b32 v6, v65, v8, 15 bitop3:0x6c
	v_lshl_add_u32 v6, v6, 4, v71
	v_or_b32_e32 v6, v6, v57
	v_add_u32_e32 v7, 0, v6
	ds_write_b16_d16_hi v7, v4
	v_add_u32_e32 v4, s1, v6
	ds_write_b16_d16_hi v4, v5
	s_waitcnt vmcnt(0)
	v_bfe_u32 v5, v0, 16, 1
	v_add3_u32 v5, v0, v5, s0
	v_and_b32_e32 v6, 0xffff0000, v5
	v_sub_f32_e32 v0, v0, v6
	v_ashrrev_i32_e32 v4, 8, v60
	v_bfe_u32 v6, v0, 16, 1
	v_add3_u32 v0, v0, v6, s0
	v_bitop3_b32 v6, v4, v58, 12 bitop3:0x78
	v_lshl_add_u32 v6, v6, 4, v63
	v_or_b32_e32 v6, v6, v57
	v_add_u32_e32 v7, 0, v6
	ds_write_b16_d16_hi v7, v5
	v_add_u32_e32 v5, s1, v6
	ds_write_b16_d16_hi v5, v0
	v_bfe_u32 v0, v1, 16, 1
	v_add3_u32 v0, v1, v0, s0
	v_and_b32_e32 v5, 0xffff0000, v0
	v_sub_f32_e32 v1, v1, v5
	v_bfe_u32 v5, v1, 16, 1
	v_add3_u32 v1, v1, v5, s0
	v_bitop3_b32 v5, v59, v4, 13 bitop3:0x6c
	v_lshl_add_u32 v5, v5, 4, v67
	v_or_b32_e32 v5, v5, v57
	v_add_u32_e32 v6, 0, v5
	ds_write_b16_d16_hi v6, v0
	v_add_u32_e32 v0, s1, v5
	ds_write_b16_d16_hi v0, v1
	v_bfe_u32 v0, v2, 16, 1
	v_add3_u32 v0, v2, v0, s0
	v_and_b32_e32 v1, 0xffff0000, v0
	v_sub_f32_e32 v1, v2, v1
	v_bfe_u32 v2, v1, 16, 1
	v_add3_u32 v1, v1, v2, s0
	v_bitop3_b32 v2, v61, v4, 14 bitop3:0x6c
	v_lshl_add_u32 v2, v2, 4, v69
	v_or_b32_e32 v2, v2, v57
	v_add_u32_e32 v5, 0, v2
	ds_write_b16_d16_hi v5, v0
	v_add_u32_e32 v0, s1, v2
	ds_write_b16_d16_hi v0, v1
	v_bfe_u32 v0, v3, 16, 1
	v_add3_u32 v0, v3, v0, s0
	v_and_b32_e32 v1, 0xffff0000, v0
	v_sub_f32_e32 v1, v3, v1
	v_bfe_u32 v2, v1, 16, 1
	v_add3_u32 v1, v1, v2, s0
	v_bitop3_b32 v2, v65, v4, 15 bitop3:0x6c
	v_lshl_add_u32 v2, v2, 4, v71
	s_mul_i32 s60, s18, s4
	v_or_b32_e32 v2, v2, v57
	s_min_i32 s4, s60, 0x8000
	s_movk_i32 s5, 0x800
	v_add_u32_e32 v3, 0, v2
	ds_write_b16_d16_hi v3, v0
	v_add_u32_e32 v0, s1, v2
	s_ashr_i32 s65, s4, 11
	v_cmp_gt_i32_e32 vcc, s5, v56
	ds_write_b16_d16_hi v0, v1
	s_and_saveexec_b64 s[0:1], vcc
	s_cbranch_execz .LBB0_1657
	s_add_u32 s4, s52, 0x34811000
	s_addc_u32 s5, s53, 0
	s_add_i32 s6, s60, s18
	s_min_i32 s6, s6, 0x8001
	v_max_i32_e32 v0, 0x600, v56
	s_add_i32 s6, s6, -1
	v_sub_u32_e32 v0, v0, v56
	s_ashr_i32 s12, s6, 11
	s_movk_i32 s6, 0x1ff
	v_add_u32_e32 v1, 0x1ff, v0
	v_cmp_lt_u32_e32 vcc, s6, v1
	s_mov_b64 s[8:9], -1
	v_mov_b32_e32 v0, v56
	s_and_saveexec_b64 s[6:7], vcc
	s_cbranch_execz .LBB0_1654
	v_lshrrev_b32_e32 v2, 9, v1
	v_add_u32_e32 v0, -1, v2
	v_add_u32_e32 v57, 0x200, v56
	v_lshrrev_b32_e32 v1, 1, v0
	v_add_u32_e32 v3, 1, v1
	v_cmp_lt_u32_e32 vcc, 5, v0
	v_mov_b32_e32 v10, 0
	v_mov_b64_e32 v[0:1], v[56:57]
	s_and_saveexec_b64 s[8:9], vcc
	s_cbranch_execz .LBB0_1648
	s_lshl_b32 s10, s94, 8
	s_add_i32 s10, s10, 0
	v_lshl_add_u32 v0, v92, 2, s10
	v_and_b32_e32 v4, -4, v3
	s_mov_b32 s13, 0
	v_add_u32_e32 v5, 0x20000, v0
	s_mov_b64 s[10:11], 0
	s_movk_i32 s14, 0x400
	v_mov_b32_e32 v6, s12
	v_mov_b32_e32 v7, s65
	v_mov_b32_e32 v8, s12
	v_mov_b32_e32 v9, s65
	s_movk_i32 s15, 0xfbff
	s_movk_i32 s16, 0xf800
	s_movk_i32 s17, 0xf400
	v_mov_b64_e32 v[0:1], v[56:57]

.LBB0_1769:
	s_or_b64 exec, exec, s[0:1]
	s_setprio 0
	v_readlane_b32 s4, v243, 7
	v_readlane_b32 s5, v243, 8
	s_load_dwordx4 s[0:3], s[4:5], 0x138
	v_readlane_b32 s60, v243, 10
	v_readlane_b32 s61, v243, 11
	s_waitcnt lgkmcnt(0)
	s_cmp_lt_i32 s1, 15
	s_mov_b64 s[0:1], -1
	s_cbranch_scc0 .LBB0_1771
	s_waitcnt vmcnt(0)
	s_barrier
	s_mov_b64 s[0:1], 0
